# E2: hoist token-1 expert gathers and x/g2 loads earlier (software prefetch), counted vmcnt
# speedup vs baseline: 1.0047x; 1.0047x over previous
.LBB0_886:
	s_or_b64 exec, exec, s[0:1]
	v_mov_b32_e32 v2, s92
	s_waitcnt lgkmcnt(0)
	s_barrier
	ds_read_b32 v2, v2
	s_mov_b64 s[0:1], -1
	s_waitcnt lgkmcnt(0)
	v_readfirstlane_b32 s2, v2
	s_cmp_ge_i32 s2, s60
	s_cbranch_scc1 .LBB0_881
	s_and_b32 s0, s2, 0xffffff00
	s_lshl_b32 s3, s2, 6
	s_add_i32 s2, s0, 0x100
	s_and_b64 s[0:1], s[30:31], exec
	v_mov_b32_e32 v14, v0
	s_cselect_b32 s0, 0, s2
	s_add_i32 s0, s0, s3
	v_ashrrev_i32_e32 v2, 3, v14
	v_and_b32_e32 v2, -8, v2
	v_add_u32_e32 v112, s0, v2
	v_lshlrev_b32_e32 v2, 2, v14
	v_and_b32_e32 v10, 0xe0, v2
	v_or_b32_e32 v2, 1, v112
	v_mov_b32_e32 v11, v211
	v_ashrrev_i32_e32 v113, 31, v112
	v_ashrrev_i32_e32 v3, 31, v2
	v_lshl_add_u64 v[114:115], s[22:23], 0, v[10:11]
	v_lshlrev_b64 v[12:13], 8, v[112:113]
	v_lshlrev_b64 v[2:3], 8, v[2:3]
	v_lshl_add_u64 v[6:7], v[114:115], 0, v[12:13]
	v_lshl_add_u64 v[2:3], v[114:115], 0, v[2:3]
	global_load_dwordx4 v[80:83], v[2:3], off offset:16
	global_load_dwordx4 v[40:43], v[2:3], off
	s_nop 0
	global_load_dwordx4 v[2:5], v[6:7], off offset:16
	s_nop 0
	global_load_dwordx4 v[6:9], v[6:7], off
	v_and_b32_e32 v11, 7, v14
	v_bfe_u32 v15, v14, 3, 1
	v_lshrrev_b32_e32 v14, 1, v14
	v_lshlrev_b32_e32 v210, 4, v11
	v_cmp_eq_u32_e64 s[38:39], 0, v15
	v_lshl_or_b32 v11, v11, 5, s58
	v_and_b32_e32 v14, 24, v14
	v_lshlrev_b32_e32 v15, 2, v15
	v_or_b32_e32 v12, v12, v10
	v_or3_b32 v118, v11, v14, v15
	v_lshl_add_u64 v[120:121], s[56:57], 0, v[12:13]
	s_mov_b32 s33, 0
	v_lshl_add_u64 v[116:117], s[40:41], 0, v[210:211]
	s_waitcnt vmcnt(3)
	v_mov_b64_e32 v[10:11], v[80:81]
	s_waitcnt vmcnt(2)
	v_mov_b64_e32 v[14:15], v[40:41]
	v_mov_b64_e32 v[12:13], v[82:83]
	v_mov_b64_e32 v[16:17], v[42:43]
	s_waitcnt vmcnt(0)
	s_branch .LBB0_889
.LBB0_888:
	s_or_b64 exec, exec, s[0:1]
	v_mul_i32_i24_e32 v35, 0x3000, v35
	v_cndmask_b32_e32 v38, v35, v223, vcc
	v_ashrrev_i32_e32 v39, 31, v38
	v_lshl_add_u64 v[38:39], v[38:39], 2, s[10:11]
	v_ashrrev_i32_e32 v35, 31, v34
	v_lshl_add_u64 v[38:39], v[38:39], 0, v[210:211]
	v_lshlrev_b64 v[34:35], 13, v[34:35]
	v_lshl_add_u64 v[34:35], v[36:37], 0, v[34:35]
	v_add_co_u32_e32 v38, vcc, s94, v38
	v_lshl_add_u64 v[48:49], v[34:35], 0, v[210:211]
	s_nop 0
	v_addc_co_u32_e32 v39, vcc, 0, v39, vcc
	v_pk_add_f32 v[20:21], v[20:21], v[24:25]
	v_pk_add_f32 v[24:25], v[28:29], v[32:33]
	v_pk_add_f32 v[18:19], v[18:19], v[22:23]
	v_pk_add_f32 v[22:23], v[26:27], v[30:31]
	v_mov_b64_e32 v[82:83], v[12:13]
	v_mov_b64_e32 v[42:43], v[16:17]
	v_cndmask_b32_e64 v23, v23, v25, s[38:39]
	v_cndmask_b32_e64 v22, v22, v24, s[38:39]
	v_cndmask_b32_e64 v19, v19, v21, s[38:39]
	v_cndmask_b32_e64 v18, v18, v20, s[38:39]
	s_add_i32 s33, s33, 2
	v_lshl_add_u64 v[120:121], v[120:121], 0, s[82:83]
	s_and_b64 vcc, exec, s[42:43]
	v_mov_b64_e32 v[80:81], v[10:11]
	v_mov_b64_e32 v[40:41], v[14:15]
	s_waitcnt vmcnt(0)
	v_pk_fma_f32 v[18:19], v[238:239], v[18:19], v[234:235]
	v_pk_fma_f32 v[20:21], v[240:241], v[22:23], v[236:237]
	global_store_dwordx4 v[48:49], v[18:21], off
	s_cbranch_vccnz .LBB0_880
.LBB0_889:
	s_waitcnt vmcnt(1)
	v_lshlrev_b32_e32 v18, 7, v6
	v_and_b32_e32 v210, 0x7fff80, v18
	v_lshl_add_u64 v[18:19], v[116:117], 0, v[210:211]
	v_lshlrev_b32_sdwa v210, v230, v6 dst_sel:DWORD dst_unused:UNUSED_PAD src0_sel:DWORD src1_sel:WORD_1
	v_lshl_add_u64 v[20:21], v[116:117], 0, v[210:211]
	global_load_dwordx4 v[108:111], v[18:19], off
	global_load_dwordx4 v[104:107], v[20:21], off
	v_lshlrev_b32_e32 v18, 7, v7
	v_and_b32_e32 v210, 0x7fff80, v18
	v_lshl_add_u64 v[18:19], v[116:117], 0, v[210:211]
	v_lshlrev_b32_sdwa v210, v230, v7 dst_sel:DWORD dst_unused:UNUSED_PAD src0_sel:DWORD src1_sel:WORD_1
	v_lshl_add_u64 v[20:21], v[116:117], 0, v[210:211]
	global_load_dwordx4 v[100:103], v[18:19], off
	global_load_dwordx4 v[44:47], v[20:21], off
	v_lshlrev_b32_e32 v18, 7, v8
	v_and_b32_e32 v210, 0x7fff80, v18
	v_lshl_add_u64 v[18:19], v[116:117], 0, v[210:211]
	v_lshlrev_b32_sdwa v210, v230, v8 dst_sel:DWORD dst_unused:UNUSED_PAD src0_sel:DWORD src1_sel:WORD_1
	v_lshl_add_u64 v[20:21], v[116:117], 0, v[210:211]
	global_load_dwordx4 v[34:37], v[18:19], off
	global_load_dwordx4 v[26:29], v[20:21], off
	v_lshlrev_b32_e32 v18, 7, v9
	v_and_b32_e32 v210, 0x7fff80, v18
	v_lshl_add_u64 v[18:19], v[116:117], 0, v[210:211]
	v_lshlrev_b32_sdwa v210, v230, v9 dst_sel:DWORD dst_unused:UNUSED_PAD src0_sel:DWORD src1_sel:WORD_1
	v_lshlrev_b32_e32 v30, 7, v2
	v_lshl_add_u64 v[20:21], v[116:117], 0, v[210:211]
	v_and_b32_e32 v210, 0x7fff80, v30
	v_lshl_add_u64 v[30:31], v[116:117], 0, v[210:211]
	v_lshlrev_b32_sdwa v210, v230, v2 dst_sel:DWORD dst_unused:UNUSED_PAD src0_sel:DWORD src1_sel:WORD_1
	global_load_dwordx4 v[22:25], v[18:19], off
	s_nop 0
	global_load_dwordx4 v[18:21], v[20:21], off
	v_lshl_add_u64 v[32:33], v[116:117], 0, v[210:211]
	global_load_dwordx4 v[96:99], v[30:31], off
	global_load_dwordx4 v[92:95], v[32:33], off
	v_lshlrev_b32_e32 v30, 7, v3
	v_and_b32_e32 v210, 0x7fff80, v30
	v_lshl_add_u64 v[30:31], v[116:117], 0, v[210:211]
	v_lshlrev_b32_sdwa v210, v230, v3 dst_sel:DWORD dst_unused:UNUSED_PAD src0_sel:DWORD src1_sel:WORD_1
	v_lshl_add_u64 v[32:33], v[116:117], 0, v[210:211]
	global_load_dwordx4 v[84:87], v[30:31], off
	global_load_dwordx4 v[74:77], v[32:33], off
	v_lshlrev_b32_e32 v30, 7, v4
	v_and_b32_e32 v210, 0x7fff80, v30
	v_lshl_add_u64 v[30:31], v[116:117], 0, v[210:211]
	v_lshlrev_b32_sdwa v210, v230, v4 dst_sel:DWORD dst_unused:UNUSED_PAD src0_sel:DWORD src1_sel:WORD_1
	v_lshl_add_u64 v[32:33], v[116:117], 0, v[210:211]
	global_load_dwordx4 v[70:73], v[30:31], off
	global_load_dwordx4 v[66:69], v[32:33], off
	v_lshlrev_b32_e32 v30, 7, v5
	v_and_b32_e32 v210, 0x7fff80, v30
	v_lshl_add_u64 v[30:31], v[116:117], 0, v[210:211]
	v_lshlrev_b32_sdwa v210, v230, v5 dst_sel:DWORD dst_unused:UNUSED_PAD src0_sel:DWORD src1_sel:WORD_1
	v_lshl_add_u64 v[32:33], v[116:117], 0, v[210:211]
	global_load_dwordx4 v[58:61], v[30:31], off
	global_load_dwordx4 v[88:91], v[32:33], off
	global_load_dwordx4 v[62:65], v[120:121], off offset:-256
	s_nop 0
	global_load_dwordx4 v[30:33], v[120:121], off offset:-272
	global_load_dwordx4 v[54:57], v[120:121], off
	global_load_dwordx4 v[50:53], v[120:121], off offset:-16
	v_lshlrev_b32_e32 v192, 7, v40
	v_and_b32_e32 v210, 0x7fff80, v192
	v_lshl_add_u64 v[192:193], v[116:117], 0, v[210:211]
	v_lshlrev_b32_sdwa v210, v230, v40 dst_sel:DWORD dst_unused:UNUSED_PAD src0_sel:DWORD src1_sel:WORD_1
	v_lshl_add_u64 v[194:195], v[116:117], 0, v[210:211]
	global_load_dwordx4 v[128:131], v[192:193], off
	global_load_dwordx4 v[132:135], v[194:195], off
	v_lshlrev_b32_e32 v192, 7, v41
	v_and_b32_e32 v210, 0x7fff80, v192
	v_lshl_add_u64 v[192:193], v[116:117], 0, v[210:211]
	v_lshlrev_b32_sdwa v210, v230, v41 dst_sel:DWORD dst_unused:UNUSED_PAD src0_sel:DWORD src1_sel:WORD_1
	v_lshl_add_u64 v[194:195], v[116:117], 0, v[210:211]
	global_load_dwordx4 v[136:139], v[192:193], off
	global_load_dwordx4 v[140:143], v[194:195], off
	v_lshlrev_b32_e32 v192, 7, v42
	v_and_b32_e32 v210, 0x7fff80, v192
	v_lshl_add_u64 v[192:193], v[116:117], 0, v[210:211]
	v_lshlrev_b32_sdwa v210, v230, v42 dst_sel:DWORD dst_unused:UNUSED_PAD src0_sel:DWORD src1_sel:WORD_1
	v_lshl_add_u64 v[194:195], v[116:117], 0, v[210:211]
	global_load_dwordx4 v[144:147], v[192:193], off
	global_load_dwordx4 v[148:151], v[194:195], off
	v_lshlrev_b32_e32 v192, 7, v43
	v_and_b32_e32 v210, 0x7fff80, v192
	v_lshl_add_u64 v[192:193], v[116:117], 0, v[210:211]
	v_lshlrev_b32_sdwa v210, v230, v43 dst_sel:DWORD dst_unused:UNUSED_PAD src0_sel:DWORD src1_sel:WORD_1
	v_lshl_add_u64 v[194:195], v[116:117], 0, v[210:211]
	global_load_dwordx4 v[152:155], v[192:193], off
	global_load_dwordx4 v[156:159], v[194:195], off
	v_lshlrev_b32_e32 v192, 7, v80
	v_and_b32_e32 v210, 0x7fff80, v192
	v_lshl_add_u64 v[192:193], v[116:117], 0, v[210:211]
	v_lshlrev_b32_sdwa v210, v230, v80 dst_sel:DWORD dst_unused:UNUSED_PAD src0_sel:DWORD src1_sel:WORD_1
	v_lshl_add_u64 v[194:195], v[116:117], 0, v[210:211]
	global_load_dwordx4 v[160:163], v[192:193], off
	global_load_dwordx4 v[164:167], v[194:195], off
	v_lshlrev_b32_e32 v192, 7, v81
	v_and_b32_e32 v210, 0x7fff80, v192
	v_lshl_add_u64 v[192:193], v[116:117], 0, v[210:211]
	v_lshlrev_b32_sdwa v210, v230, v81 dst_sel:DWORD dst_unused:UNUSED_PAD src0_sel:DWORD src1_sel:WORD_1
	v_lshl_add_u64 v[194:195], v[116:117], 0, v[210:211]
	global_load_dwordx4 v[168:171], v[192:193], off
	global_load_dwordx4 v[172:175], v[194:195], off
	v_lshlrev_b32_e32 v192, 7, v82
	v_and_b32_e32 v210, 0x7fff80, v192
	v_lshl_add_u64 v[192:193], v[116:117], 0, v[210:211]
	v_lshlrev_b32_sdwa v210, v230, v82 dst_sel:DWORD dst_unused:UNUSED_PAD src0_sel:DWORD src1_sel:WORD_1
	v_lshl_add_u64 v[194:195], v[116:117], 0, v[210:211]
	global_load_dwordx4 v[176:179], v[192:193], off
	global_load_dwordx4 v[180:183], v[194:195], off
	v_lshlrev_b32_e32 v192, 7, v83
	v_and_b32_e32 v210, 0x7fff80, v192
	v_lshl_add_u64 v[192:193], v[116:117], 0, v[210:211]
	v_lshlrev_b32_sdwa v210, v230, v83 dst_sel:DWORD dst_unused:UNUSED_PAD src0_sel:DWORD src1_sel:WORD_1
	v_lshl_add_u64 v[194:195], v[116:117], 0, v[210:211]
	global_load_dwordx4 v[184:187], v[192:193], off
	global_load_dwordx4 v[188:191], v[194:195], off
	s_cmp_gt_u32 s33, 5
	s_cselect_b64 s[42:43], -1, 0
	v_add_u32_e32 v113, s33, v112
	s_and_b64 vcc, exec, s[42:43]
	s_cbranch_vccnz .LBB0_891
	v_add_u32_e32 v2, 2, v113
	v_add_u32_e32 v10, 3, v113
	v_ashrrev_i32_e32 v3, 31, v2
	v_ashrrev_i32_e32 v11, 31, v10
	v_lshlrev_b64 v[2:3], 8, v[2:3]
	v_lshlrev_b64 v[10:11], 8, v[10:11]
	v_lshl_add_u64 v[6:7], v[114:115], 0, v[2:3]
	v_lshl_add_u64 v[14:15], v[114:115], 0, v[10:11]
	global_load_dwordx4 v[2:5], v[6:7], off offset:16
	s_nop 0
	global_load_dwordx4 v[6:9], v[6:7], off
	s_nop 0
	global_load_dwordx4 v[10:13], v[14:15], off offset:16
	s_nop 0
	global_load_dwordx4 v[14:17], v[14:15], off
.LBB0_891:
	s_waitcnt vmcnt(18)
	v_mul_hi_i32 v244, v113, s69
	v_lshrrev_b32_e32 v245, 31, v244
	v_ashrrev_i32_e32 v244, 13, v244
	v_add_u32_e32 v245, v244, v245
	v_mul_i32_i24_e32 v248, 0xffffbf00, v245
	v_add_u32_e32 v244, v113, v248
	v_cmp_gt_i32_e32 vcc, s68, v244
	v_cmp_lt_i32_e64 s[0:1], s21, v244
	s_and_saveexec_b64 s[2:3], s[0:1]
	s_xor_b64 s[0:1], exec, s[2:3]
	v_lshl_add_u32 v244, v245, 14, v248
	v_add3_u32 v244, v113, v244, s88
	s_or_saveexec_b64 s[0:1], s[0:1]
	v_mov_b64_e32 v[246:247], s[18:19]
	s_xor_b64 exec, exec, s[0:1]
	v_lshlrev_b32_e32 v244, 8, v245
	v_add3_u32 v244, v248, v113, v244
	v_mov_b64_e32 v[246:247], s[72:73]
	s_or_b64 exec, exec, s[0:1]
	v_mul_i32_i24_e32 v245, 0x3000, v245
	v_cndmask_b32_e32 v248, v245, v223, vcc
	v_ashrrev_i32_e32 v249, 31, v248
	v_lshl_add_u64 v[248:249], v[248:249], 2, s[10:11]
	v_lshlrev_b32_e32 v210, 2, v118
	v_ashrrev_i32_e32 v245, 31, v244
	v_lshl_add_u64 v[250:251], v[248:249], 0, v[210:211]
	v_lshlrev_b64 v[244:245], 13, v[244:245]
	v_lshl_add_u64 v[244:245], v[246:247], 0, v[244:245]
	v_add_co_u32_e32 v250, vcc, s94, v250
	v_lshl_add_u64 v[204:205], v[244:245], 0, v[210:211]
	s_nop 0
	v_addc_co_u32_e32 v251, vcc, 0, v251, vcc
	global_load_dwordx4 v[196:199], v[204:205], off
	global_load_dwordx4 v[200:203], v[250:251], off
	v_mul_u32_u24_sdwa v38, v30, s93 dst_sel:DWORD dst_unused:UNUSED_PAD src0_sel:WORD_0 src1_sel:DWORD
	v_cvt_scalef32_pk_f16_fp4 v39, v108, 1.0
	v_cvt_scalef32_pk_f16_fp4 v48, v108, 1.0 op_sel:[1,0,0]
	v_cvt_scalef32_pk_f16_fp4 v49, v108, 1.0 op_sel:[0,1,0]
	v_cvt_scalef32_pk_f16_fp4 v78, v108, 1.0 op_sel:[1,1,0]
	v_cvt_scalef32_pk_f16_fp4 v79, v109, 1.0
	v_cvt_scalef32_pk_f16_fp4 v108, v109, 1.0 op_sel:[1,0,0]
	v_cvt_scalef32_pk_f16_fp4 v119, v109, 1.0 op_sel:[0,1,0]
	v_cvt_scalef32_pk_f16_fp4 v109, v109, 1.0 op_sel:[1,1,0]
	v_cvt_scalef32_pk_f16_fp4 v122, v110, 1.0
	v_cvt_scalef32_pk_f16_fp4 v123, v110, 1.0 op_sel:[1,0,0]
	v_cvt_scalef32_pk_f16_fp4 v124, v110, 1.0 op_sel:[0,1,0]
	v_cvt_scalef32_pk_f16_fp4 v110, v110, 1.0 op_sel:[1,1,0]
	v_cvt_scalef32_pk_f16_fp4 v125, v111, 1.0
	v_cvt_scalef32_pk_f16_fp4 v126, v111, 1.0 op_sel:[1,0,0]
	v_cvt_scalef32_pk_f16_fp4 v127, v111, 1.0 op_sel:[0,1,0]
	v_cvt_scalef32_pk_f16_fp4 v111, v111, 1.0 op_sel:[1,1,0]
	v_pk_fma_f16 v39, v39, v38, 0
	v_pk_fma_f16 v48, v48, v38, 0
	v_pk_fma_f16 v49, v49, v38, 0
	v_pk_fma_f16 v78, v78, v38, 0
	v_pk_fma_f16 v79, v79, v38, 0
	v_pk_fma_f16 v108, v108, v38, 0
	v_pk_fma_f16 v119, v119, v38, 0
	v_pk_fma_f16 v109, v109, v38, 0
	v_pk_fma_f16 v122, v122, v38, 0
	v_pk_fma_f16 v123, v123, v38, 0
	v_pk_fma_f16 v124, v124, v38, 0
	v_pk_fma_f16 v110, v110, v38, 0
	v_pk_fma_f16 v125, v125, v38, 0
	v_pk_fma_f16 v126, v126, v38, 0
	v_pk_fma_f16 v127, v127, v38, 0
	v_pk_fma_f16 v38, v111, v38, 0
	v_mul_u32_u24_sdwa v30, v30, s93 dst_sel:DWORD dst_unused:UNUSED_PAD src0_sel:WORD_1 src1_sel:DWORD
	v_cvt_scalef32_pk_f16_fp4 v111, v104, 1.0
	v_pk_fma_f16 v39, v111, v30, v39
	v_cvt_scalef32_pk_f16_fp4 v111, v104, 1.0 op_sel:[1,0,0]
	v_pk_fma_f16 v48, v111, v30, v48
	v_cvt_scalef32_pk_f16_fp4 v111, v104, 1.0 op_sel:[0,1,0]
	v_cvt_scalef32_pk_f16_fp4 v104, v104, 1.0 op_sel:[1,1,0]
	v_pk_fma_f16 v78, v104, v30, v78
	v_cvt_scalef32_pk_f16_fp4 v104, v105, 1.0
	v_pk_fma_f16 v79, v104, v30, v79
	v_cvt_scalef32_pk_f16_fp4 v104, v105, 1.0 op_sel:[1,0,0]
	v_pk_fma_f16 v104, v104, v30, v108
	v_cvt_scalef32_pk_f16_fp4 v108, v105, 1.0 op_sel:[0,1,0]
	v_cvt_scalef32_pk_f16_fp4 v105, v105, 1.0 op_sel:[1,1,0]
	v_pk_fma_f16 v49, v111, v30, v49
	v_pk_fma_f16 v108, v108, v30, v119
	v_pk_fma_f16 v105, v105, v30, v109
	v_cvt_scalef32_pk_f16_fp4 v109, v106, 1.0
	v_cvt_scalef32_pk_f16_fp4 v111, v106, 1.0 op_sel:[1,0,0]
	v_cvt_scalef32_pk_f16_fp4 v119, v106, 1.0 op_sel:[0,1,0]
	v_cvt_scalef32_pk_f16_fp4 v106, v106, 1.0 op_sel:[1,1,0]
	v_pk_fma_f16 v109, v109, v30, v122
	v_pk_fma_f16 v111, v111, v30, v123
	v_pk_fma_f16 v106, v106, v30, v110
	v_cvt_scalef32_pk_f16_fp4 v110, v107, 1.0
	v_cvt_scalef32_pk_f16_fp4 v122, v107, 1.0 op_sel:[1,0,0]
	v_cvt_scalef32_pk_f16_fp4 v123, v107, 1.0 op_sel:[0,1,0]
	v_cvt_scalef32_pk_f16_fp4 v107, v107, 1.0 op_sel:[1,1,0]
	v_pk_fma_f16 v119, v119, v30, v124
	v_pk_fma_f16 v110, v110, v30, v125
	v_pk_fma_f16 v122, v122, v30, v126
	v_pk_fma_f16 v123, v123, v30, v127
	v_pk_fma_f16 v30, v107, v30, v38
	v_mul_u32_u24_sdwa v38, v31, s93 dst_sel:DWORD dst_unused:UNUSED_PAD src0_sel:WORD_0 src1_sel:DWORD
	v_cvt_scalef32_pk_f16_fp4 v107, v100, 1.0
	v_pk_fma_f16 v39, v107, v38, v39
	v_cvt_scalef32_pk_f16_fp4 v107, v100, 1.0 op_sel:[1,0,0]
	v_pk_fma_f16 v48, v107, v38, v48
	v_cvt_scalef32_pk_f16_fp4 v107, v100, 1.0 op_sel:[0,1,0]
	v_cvt_scalef32_pk_f16_fp4 v100, v100, 1.0 op_sel:[1,1,0]
	v_pk_fma_f16 v78, v100, v38, v78
	v_cvt_scalef32_pk_f16_fp4 v100, v101, 1.0
	v_pk_fma_f16 v79, v100, v38, v79
	v_cvt_scalef32_pk_f16_fp4 v100, v101, 1.0 op_sel:[1,0,0]
	v_pk_fma_f16 v100, v100, v38, v104
	v_cvt_scalef32_pk_f16_fp4 v104, v101, 1.0 op_sel:[0,1,0]
	v_cvt_scalef32_pk_f16_fp4 v101, v101, 1.0 op_sel:[1,1,0]
	v_pk_fma_f16 v49, v107, v38, v49
	v_pk_fma_f16 v104, v104, v38, v108
	v_pk_fma_f16 v101, v101, v38, v105
	v_cvt_scalef32_pk_f16_fp4 v105, v102, 1.0
	v_cvt_scalef32_pk_f16_fp4 v107, v102, 1.0 op_sel:[1,0,0]
	v_cvt_scalef32_pk_f16_fp4 v108, v102, 1.0 op_sel:[0,1,0]
	v_cvt_scalef32_pk_f16_fp4 v102, v102, 1.0 op_sel:[1,1,0]
	v_pk_fma_f16 v102, v102, v38, v106
	v_cvt_scalef32_pk_f16_fp4 v106, v103, 1.0
	v_pk_fma_f16 v105, v105, v38, v109
	v_pk_fma_f16 v106, v106, v38, v110
	v_cvt_scalef32_pk_f16_fp4 v109, v103, 1.0 op_sel:[1,0,0]
	v_cvt_scalef32_pk_f16_fp4 v110, v103, 1.0 op_sel:[0,1,0]
	v_cvt_scalef32_pk_f16_fp4 v103, v103, 1.0 op_sel:[1,1,0]
	v_pk_fma_f16 v107, v107, v38, v111
	v_pk_fma_f16 v108, v108, v38, v119
	v_pk_fma_f16 v109, v109, v38, v122
	v_pk_fma_f16 v110, v110, v38, v123
	v_pk_fma_f16 v30, v103, v38, v30
	v_mul_u32_u24_sdwa v31, v31, s93 dst_sel:DWORD dst_unused:UNUSED_PAD src0_sel:WORD_1 src1_sel:DWORD
	v_cvt_scalef32_pk_f16_fp4 v38, v44, 1.0
	v_pk_fma_f16 v38, v38, v31, v39
	v_cvt_scalef32_pk_f16_fp4 v39, v44, 1.0 op_sel:[1,0,0]
	v_pk_fma_f16 v39, v39, v31, v48
	v_cvt_scalef32_pk_f16_fp4 v48, v44, 1.0 op_sel:[0,1,0]
	v_pk_fma_f16 v48, v48, v31, v49
	v_cvt_scalef32_pk_f16_fp4 v44, v44, 1.0 op_sel:[1,1,0]
	v_cvt_scalef32_pk_f16_fp4 v49, v45, 1.0
	v_pk_fma_f16 v44, v44, v31, v78
	v_pk_fma_f16 v49, v49, v31, v79
	v_cvt_scalef32_pk_f16_fp4 v78, v45, 1.0 op_sel:[1,0,0]
	v_cvt_scalef32_pk_f16_fp4 v79, v45, 1.0 op_sel:[0,1,0]
	v_cvt_scalef32_pk_f16_fp4 v45, v45, 1.0 op_sel:[1,1,0]
	v_pk_fma_f16 v78, v78, v31, v100
	v_pk_fma_f16 v45, v45, v31, v101
	v_cvt_scalef32_pk_f16_fp4 v100, v46, 1.0
	v_cvt_scalef32_pk_f16_fp4 v101, v46, 1.0 op_sel:[1,0,0]
	v_cvt_scalef32_pk_f16_fp4 v103, v46, 1.0 op_sel:[0,1,0]
	v_cvt_scalef32_pk_f16_fp4 v46, v46, 1.0 op_sel:[1,1,0]
	v_pk_fma_f16 v79, v79, v31, v104
	v_pk_fma_f16 v100, v100, v31, v105
	v_pk_fma_f16 v46, v46, v31, v102
	v_cvt_scalef32_pk_f16_fp4 v102, v47, 1.0
	v_cvt_scalef32_pk_f16_fp4 v104, v47, 1.0 op_sel:[1,0,0]
	v_cvt_scalef32_pk_f16_fp4 v105, v47, 1.0 op_sel:[0,1,0]
	v_cvt_scalef32_pk_f16_fp4 v47, v47, 1.0 op_sel:[1,1,0]
	v_pk_fma_f16 v101, v101, v31, v107
	v_pk_fma_f16 v103, v103, v31, v108
	v_pk_fma_f16 v102, v102, v31, v106
	v_pk_fma_f16 v104, v104, v31, v109
	v_pk_fma_f16 v105, v105, v31, v110
	v_pk_fma_f16 v30, v47, v31, v30
	v_mul_u32_u24_sdwa v31, v32, s93 dst_sel:DWORD dst_unused:UNUSED_PAD src0_sel:WORD_0 src1_sel:DWORD
	v_cvt_scalef32_pk_f16_fp4 v47, v34, 1.0
	v_pk_fma_f16 v38, v47, v31, v38
	v_cvt_scalef32_pk_f16_fp4 v47, v34, 1.0 op_sel:[1,0,0]
	v_pk_fma_f16 v39, v47, v31, v39
	v_cvt_scalef32_pk_f16_fp4 v47, v34, 1.0 op_sel:[0,1,0]
	v_cvt_scalef32_pk_f16_fp4 v34, v34, 1.0 op_sel:[1,1,0]
	v_pk_fma_f16 v34, v34, v31, v44
	v_cvt_scalef32_pk_f16_fp4 v44, v35, 1.0
	v_pk_fma_f16 v47, v47, v31, v48
	v_pk_fma_f16 v44, v44, v31, v49
	v_cvt_scalef32_pk_f16_fp4 v48, v35, 1.0 op_sel:[1,0,0]
	v_cvt_scalef32_pk_f16_fp4 v49, v35, 1.0 op_sel:[0,1,0]
	v_cvt_scalef32_pk_f16_fp4 v35, v35, 1.0 op_sel:[1,1,0]
	v_pk_fma_f16 v48, v48, v31, v78
	v_pk_fma_f16 v49, v49, v31, v79
	v_pk_fma_f16 v35, v35, v31, v45
	v_cvt_scalef32_pk_f16_fp4 v45, v36, 1.0
	v_cvt_scalef32_pk_f16_fp4 v78, v36, 1.0 op_sel:[1,0,0]
	v_cvt_scalef32_pk_f16_fp4 v79, v36, 1.0 op_sel:[0,1,0]
	v_cvt_scalef32_pk_f16_fp4 v36, v36, 1.0 op_sel:[1,1,0]
	v_pk_fma_f16 v45, v45, v31, v100
	v_pk_fma_f16 v78, v78, v31, v101
	v_pk_fma_f16 v36, v36, v31, v46
	v_cvt_scalef32_pk_f16_fp4 v46, v37, 1.0
	v_cvt_scalef32_pk_f16_fp4 v100, v37, 1.0 op_sel:[1,0,0]
	v_cvt_scalef32_pk_f16_fp4 v101, v37, 1.0 op_sel:[0,1,0]
	v_cvt_scalef32_pk_f16_fp4 v37, v37, 1.0 op_sel:[1,1,0]
	v_pk_fma_f16 v79, v79, v31, v103
	v_pk_fma_f16 v46, v46, v31, v102
	v_pk_fma_f16 v100, v100, v31, v104
	v_pk_fma_f16 v101, v101, v31, v105
	v_pk_fma_f16 v30, v37, v31, v30
	v_mul_u32_u24_sdwa v31, v32, s93 dst_sel:DWORD dst_unused:UNUSED_PAD src0_sel:WORD_1 src1_sel:DWORD
	v_cvt_scalef32_pk_f16_fp4 v32, v26, 1.0
	v_pk_fma_f16 v32, v32, v31, v38
	v_cvt_scalef32_pk_f16_fp4 v37, v26, 1.0 op_sel:[1,0,0]
	v_cvt_scalef32_pk_f16_fp4 v38, v26, 1.0 op_sel:[0,1,0]
	v_cvt_scalef32_pk_f16_fp4 v26, v26, 1.0 op_sel:[1,1,0]
	v_pk_fma_f16 v26, v26, v31, v34
	v_cvt_scalef32_pk_f16_fp4 v34, v27, 1.0
	v_pk_fma_f16 v37, v37, v31, v39
	v_pk_fma_f16 v34, v34, v31, v44
	v_cvt_scalef32_pk_f16_fp4 v39, v27, 1.0 op_sel:[1,0,0]
	v_cvt_scalef32_pk_f16_fp4 v44, v27, 1.0 op_sel:[0,1,0]
	v_cvt_scalef32_pk_f16_fp4 v27, v27, 1.0 op_sel:[1,1,0]
	v_pk_fma_f16 v27, v27, v31, v35
	v_cvt_scalef32_pk_f16_fp4 v35, v28, 1.0
	v_pk_fma_f16 v38, v38, v31, v47
	v_pk_fma_f16 v35, v35, v31, v45
	v_cvt_scalef32_pk_f16_fp4 v45, v28, 1.0 op_sel:[1,0,0]
	v_cvt_scalef32_pk_f16_fp4 v47, v28, 1.0 op_sel:[0,1,0]
	v_cvt_scalef32_pk_f16_fp4 v28, v28, 1.0 op_sel:[1,1,0]
	v_pk_fma_f16 v28, v28, v31, v36
	v_cvt_scalef32_pk_f16_fp4 v36, v29, 1.0
	v_pk_fma_f16 v39, v39, v31, v48
	v_pk_fma_f16 v36, v36, v31, v46
	v_cvt_scalef32_pk_f16_fp4 v46, v29, 1.0 op_sel:[1,0,0]
	v_cvt_scalef32_pk_f16_fp4 v48, v29, 1.0 op_sel:[0,1,0]
	v_cvt_scalef32_pk_f16_fp4 v29, v29, 1.0 op_sel:[1,1,0]
	v_pk_fma_f16 v44, v44, v31, v49
	v_pk_fma_f16 v45, v45, v31, v78
	v_pk_fma_f16 v47, v47, v31, v79
	v_pk_fma_f16 v46, v46, v31, v100
	v_pk_fma_f16 v48, v48, v31, v101
	v_pk_fma_f16 v29, v29, v31, v30
	v_mul_u32_u24_sdwa v30, v33, s93 dst_sel:DWORD dst_unused:UNUSED_PAD src0_sel:WORD_0 src1_sel:DWORD
	v_cvt_scalef32_pk_f16_fp4 v31, v22, 1.0
	v_pk_fma_f16 v31, v31, v30, v32
	v_cvt_scalef32_pk_f16_fp4 v32, v22, 1.0 op_sel:[1,0,0]
	v_pk_fma_f16 v32, v32, v30, v37
	v_cvt_scalef32_pk_f16_fp4 v37, v22, 1.0 op_sel:[0,1,0]
	v_cvt_scalef32_pk_f16_fp4 v22, v22, 1.0 op_sel:[1,1,0]
	v_pk_fma_f16 v22, v22, v30, v26
	v_cvt_scalef32_pk_f16_fp4 v26, v23, 1.0
	v_pk_fma_f16 v37, v37, v30, v38
	v_pk_fma_f16 v26, v26, v30, v34
	v_cvt_scalef32_pk_f16_fp4 v34, v23, 1.0 op_sel:[1,0,0]
	v_cvt_scalef32_pk_f16_fp4 v38, v23, 1.0 op_sel:[0,1,0]
	v_cvt_scalef32_pk_f16_fp4 v23, v23, 1.0 op_sel:[1,1,0]
	v_pk_fma_f16 v23, v23, v30, v27
	v_cvt_scalef32_pk_f16_fp4 v27, v24, 1.0
	v_pk_fma_f16 v34, v34, v30, v39
	v_pk_fma_f16 v27, v27, v30, v35
	v_cvt_scalef32_pk_f16_fp4 v35, v24, 1.0 op_sel:[1,0,0]
	v_cvt_scalef32_pk_f16_fp4 v39, v24, 1.0 op_sel:[0,1,0]
	v_cvt_scalef32_pk_f16_fp4 v24, v24, 1.0 op_sel:[1,1,0]
	v_pk_fma_f16 v24, v24, v30, v28
	v_cvt_scalef32_pk_f16_fp4 v28, v25, 1.0
	v_pk_fma_f16 v38, v38, v30, v44
	v_pk_fma_f16 v28, v28, v30, v36
	v_cvt_scalef32_pk_f16_fp4 v36, v25, 1.0 op_sel:[1,0,0]
	v_cvt_scalef32_pk_f16_fp4 v44, v25, 1.0 op_sel:[0,1,0]
	v_cvt_scalef32_pk_f16_fp4 v25, v25, 1.0 op_sel:[1,1,0]
	v_pk_fma_f16 v35, v35, v30, v45
	v_pk_fma_f16 v39, v39, v30, v47
	v_pk_fma_f16 v36, v36, v30, v46
	v_pk_fma_f16 v44, v44, v30, v48
	v_pk_fma_f16 v25, v25, v30, v29
	v_mul_u32_u24_sdwa v29, v33, s93 dst_sel:DWORD dst_unused:UNUSED_PAD src0_sel:WORD_1 src1_sel:DWORD
	v_cvt_scalef32_pk_f16_fp4 v30, v18, 1.0
	v_pk_fma_f16 v78, v30, v29, v31
	v_cvt_scalef32_pk_f16_fp4 v30, v18, 1.0 op_sel:[1,0,0]
	v_pk_fma_f16 v79, v30, v29, v32
	v_cvt_scalef32_pk_f16_fp4 v30, v18, 1.0 op_sel:[0,1,0]
	v_cvt_scalef32_pk_f16_fp4 v18, v18, 1.0 op_sel:[1,1,0]
	v_pk_fma_f16 v101, v18, v29, v22
	v_cvt_scalef32_pk_f16_fp4 v18, v19, 1.0
	v_pk_fma_f16 v102, v18, v29, v26
	v_cvt_scalef32_pk_f16_fp4 v18, v19, 1.0 op_sel:[1,0,0]
	v_pk_fma_f16 v103, v18, v29, v34
	v_cvt_scalef32_pk_f16_fp4 v18, v19, 1.0 op_sel:[0,1,0]
	v_mul_u32_u24_sdwa v123, v62, s93 dst_sel:DWORD dst_unused:UNUSED_PAD src0_sel:WORD_0 src1_sel:DWORD
	v_cvt_scalef32_pk_f16_fp4 v124, v96, 1.0
	v_pk_fma_f16 v104, v18, v29, v38
	v_cvt_scalef32_pk_f16_fp4 v18, v19, 1.0 op_sel:[1,1,0]
	v_pk_fma_f16 v78, v124, v123, v78
	v_cvt_scalef32_pk_f16_fp4 v124, v96, 1.0 op_sel:[1,0,0]
	v_pk_fma_f16 v105, v18, v29, v23
	v_cvt_scalef32_pk_f16_fp4 v18, v20, 1.0
	v_pk_fma_f16 v79, v124, v123, v79
	v_cvt_scalef32_pk_f16_fp4 v124, v96, 1.0 op_sel:[0,1,0]
	v_cvt_scalef32_pk_f16_fp4 v96, v96, 1.0 op_sel:[1,1,0]
	v_pk_fma_f16 v106, v18, v29, v27
	v_cvt_scalef32_pk_f16_fp4 v18, v20, 1.0 op_sel:[1,0,0]
	v_pk_fma_f16 v96, v96, v123, v101
	v_cvt_scalef32_pk_f16_fp4 v101, v97, 1.0
	v_pk_fma_f16 v107, v18, v29, v35
	v_cvt_scalef32_pk_f16_fp4 v18, v20, 1.0 op_sel:[0,1,0]
	v_pk_fma_f16 v101, v101, v123, v102
	v_cvt_scalef32_pk_f16_fp4 v102, v97, 1.0 op_sel:[1,0,0]
	v_pk_fma_f16 v108, v18, v29, v39
	v_cvt_scalef32_pk_f16_fp4 v18, v20, 1.0 op_sel:[1,1,0]
	v_pk_fma_f16 v102, v102, v123, v103
	v_cvt_scalef32_pk_f16_fp4 v103, v97, 1.0 op_sel:[0,1,0]
	v_cvt_scalef32_pk_f16_fp4 v97, v97, 1.0 op_sel:[1,1,0]
	v_pk_fma_f16 v109, v18, v29, v24
	v_cvt_scalef32_pk_f16_fp4 v18, v21, 1.0
	v_pk_fma_f16 v97, v97, v123, v105
	v_cvt_scalef32_pk_f16_fp4 v105, v98, 1.0 op_sel:[1,0,0]
	v_pk_fma_f16 v110, v18, v29, v28
	v_pk_fma_f16 v105, v105, v123, v107
	v_cvt_scalef32_pk_f16_fp4 v107, v99, 1.0
	v_pk_fma_f16 v107, v107, v123, v110
	v_mul_u32_u24_sdwa v62, v62, s93 dst_sel:DWORD dst_unused:UNUSED_PAD src0_sel:WORD_1 src1_sel:DWORD
	v_cvt_scalef32_pk_f16_fp4 v110, v92, 1.0
	v_pk_fma_f16 v78, v110, v62, v78
	v_cvt_scalef32_pk_f16_fp4 v110, v92, 1.0 op_sel:[1,0,0]
	v_pk_fma_f16 v79, v110, v62, v79
	v_cvt_scalef32_pk_f16_fp4 v110, v92, 1.0 op_sel:[0,1,0]
	v_cvt_scalef32_pk_f16_fp4 v92, v92, 1.0 op_sel:[1,1,0]
	v_pk_fma_f16 v92, v92, v62, v96
	v_cvt_scalef32_pk_f16_fp4 v96, v93, 1.0
	v_cvt_scalef32_pk_f16_fp4 v18, v21, 1.0 op_sel:[1,0,0]
	v_pk_fma_f16 v96, v96, v62, v101
	v_cvt_scalef32_pk_f16_fp4 v101, v93, 1.0 op_sel:[1,0,0]
	v_pk_fma_f16 v111, v18, v29, v36
	v_cvt_scalef32_pk_f16_fp4 v18, v21, 1.0 op_sel:[0,1,0]
	v_pk_fma_f16 v103, v103, v123, v104
	v_cvt_scalef32_pk_f16_fp4 v104, v98, 1.0
	v_pk_fma_f16 v101, v101, v62, v102
	v_cvt_scalef32_pk_f16_fp4 v102, v93, 1.0 op_sel:[0,1,0]
	v_cvt_scalef32_pk_f16_fp4 v93, v93, 1.0 op_sel:[1,1,0]
	v_pk_fma_f16 v119, v18, v29, v44
	v_cvt_scalef32_pk_f16_fp4 v18, v21, 1.0 op_sel:[1,1,0]
	v_pk_fma_f16 v104, v104, v123, v106
	v_cvt_scalef32_pk_f16_fp4 v106, v98, 1.0 op_sel:[0,1,0]
	v_cvt_scalef32_pk_f16_fp4 v98, v98, 1.0 op_sel:[1,1,0]
	v_pk_fma_f16 v93, v93, v62, v97
	v_cvt_scalef32_pk_f16_fp4 v97, v94, 1.0
	v_pk_fma_f16 v100, v30, v29, v37
	v_pk_fma_f16 v122, v18, v29, v25
	v_pk_fma_f16 v106, v106, v123, v108
	v_pk_fma_f16 v98, v98, v123, v109
	v_cvt_scalef32_pk_f16_fp4 v108, v99, 1.0 op_sel:[1,0,0]
	v_cvt_scalef32_pk_f16_fp4 v109, v99, 1.0 op_sel:[0,1,0]
	v_cvt_scalef32_pk_f16_fp4 v99, v99, 1.0 op_sel:[1,1,0]
	v_pk_fma_f16 v102, v102, v62, v103
	v_pk_fma_f16 v97, v97, v62, v104
	v_cvt_scalef32_pk_f16_fp4 v103, v94, 1.0 op_sel:[1,0,0]
	v_cvt_scalef32_pk_f16_fp4 v104, v94, 1.0 op_sel:[0,1,0]
	v_cvt_scalef32_pk_f16_fp4 v94, v94, 1.0 op_sel:[1,1,0]
	v_pk_fma_f16 v100, v124, v123, v100
	v_pk_fma_f16 v108, v108, v123, v111
	v_pk_fma_f16 v109, v109, v123, v119
	v_pk_fma_f16 v99, v99, v123, v122
	v_pk_fma_f16 v103, v103, v62, v105
	v_pk_fma_f16 v104, v104, v62, v106
	v_pk_fma_f16 v94, v94, v62, v98
	v_cvt_scalef32_pk_f16_fp4 v98, v95, 1.0
	v_cvt_scalef32_pk_f16_fp4 v105, v95, 1.0 op_sel:[1,0,0]
	v_cvt_scalef32_pk_f16_fp4 v106, v95, 1.0 op_sel:[0,1,0]
	v_cvt_scalef32_pk_f16_fp4 v95, v95, 1.0 op_sel:[1,1,0]
	v_pk_fma_f16 v100, v110, v62, v100
	v_pk_fma_f16 v98, v98, v62, v107
	v_pk_fma_f16 v105, v105, v62, v108
	v_pk_fma_f16 v106, v106, v62, v109
	v_pk_fma_f16 v62, v95, v62, v99
	v_mul_u32_u24_sdwa v95, v63, s93 dst_sel:DWORD dst_unused:UNUSED_PAD src0_sel:WORD_0 src1_sel:DWORD
	v_cvt_scalef32_pk_f16_fp4 v99, v84, 1.0
	v_pk_fma_f16 v78, v99, v95, v78
	v_cvt_scalef32_pk_f16_fp4 v99, v84, 1.0 op_sel:[1,0,0]
	v_pk_fma_f16 v79, v99, v95, v79
	v_cvt_scalef32_pk_f16_fp4 v99, v84, 1.0 op_sel:[0,1,0]
	v_cvt_scalef32_pk_f16_fp4 v84, v84, 1.0 op_sel:[1,1,0]
	v_pk_fma_f16 v84, v84, v95, v92
	v_cvt_scalef32_pk_f16_fp4 v92, v85, 1.0
	v_pk_fma_f16 v99, v99, v95, v100
	v_pk_fma_f16 v92, v92, v95, v96
	v_cvt_scalef32_pk_f16_fp4 v96, v85, 1.0 op_sel:[1,0,0]
	v_cvt_scalef32_pk_f16_fp4 v100, v85, 1.0 op_sel:[0,1,0]
	v_cvt_scalef32_pk_f16_fp4 v85, v85, 1.0 op_sel:[1,1,0]
	v_pk_fma_f16 v85, v85, v95, v93
	v_cvt_scalef32_pk_f16_fp4 v93, v86, 1.0
	v_pk_fma_f16 v96, v96, v95, v101
	v_pk_fma_f16 v93, v93, v95, v97
	v_cvt_scalef32_pk_f16_fp4 v97, v86, 1.0 op_sel:[1,0,0]
	v_cvt_scalef32_pk_f16_fp4 v101, v86, 1.0 op_sel:[0,1,0]
	v_cvt_scalef32_pk_f16_fp4 v86, v86, 1.0 op_sel:[1,1,0]
	v_pk_fma_f16 v86, v86, v95, v94
	v_cvt_scalef32_pk_f16_fp4 v94, v87, 1.0
	v_pk_fma_f16 v100, v100, v95, v102
	v_pk_fma_f16 v94, v94, v95, v98
	v_cvt_scalef32_pk_f16_fp4 v98, v87, 1.0 op_sel:[1,0,0]
	v_cvt_scalef32_pk_f16_fp4 v102, v87, 1.0 op_sel:[0,1,0]
	v_cvt_scalef32_pk_f16_fp4 v87, v87, 1.0 op_sel:[1,1,0]
	v_pk_fma_f16 v62, v87, v95, v62
	v_mul_u32_u24_sdwa v63, v63, s93 dst_sel:DWORD dst_unused:UNUSED_PAD src0_sel:WORD_1 src1_sel:DWORD
	v_cvt_scalef32_pk_f16_fp4 v87, v74, 1.0
	v_pk_fma_f16 v78, v87, v63, v78
	v_cvt_scalef32_pk_f16_fp4 v87, v74, 1.0 op_sel:[1,0,0]
	v_pk_fma_f16 v79, v87, v63, v79
	v_cvt_scalef32_pk_f16_fp4 v87, v74, 1.0 op_sel:[0,1,0]
	v_cvt_scalef32_pk_f16_fp4 v74, v74, 1.0 op_sel:[1,1,0]
	v_pk_fma_f16 v74, v74, v63, v84
	v_cvt_scalef32_pk_f16_fp4 v84, v75, 1.0
	v_pk_fma_f16 v97, v97, v95, v103
	v_pk_fma_f16 v101, v101, v95, v104
	v_pk_fma_f16 v98, v98, v95, v105
	v_pk_fma_f16 v102, v102, v95, v106
	v_pk_fma_f16 v84, v84, v63, v92
	v_cvt_scalef32_pk_f16_fp4 v92, v75, 1.0 op_sel:[1,0,0]
	v_cvt_scalef32_pk_f16_fp4 v95, v75, 1.0 op_sel:[0,1,0]
	v_cvt_scalef32_pk_f16_fp4 v75, v75, 1.0 op_sel:[1,1,0]
	v_pk_fma_f16 v75, v75, v63, v85
	v_cvt_scalef32_pk_f16_fp4 v85, v76, 1.0
	v_pk_fma_f16 v92, v92, v63, v96
	v_pk_fma_f16 v85, v85, v63, v93
	v_cvt_scalef32_pk_f16_fp4 v93, v76, 1.0 op_sel:[1,0,0]
	v_cvt_scalef32_pk_f16_fp4 v96, v76, 1.0 op_sel:[0,1,0]
	v_cvt_scalef32_pk_f16_fp4 v76, v76, 1.0 op_sel:[1,1,0]
	v_pk_fma_f16 v76, v76, v63, v86
	v_cvt_scalef32_pk_f16_fp4 v86, v77, 1.0
	v_pk_fma_f16 v93, v93, v63, v97
	v_pk_fma_f16 v86, v86, v63, v94
	v_cvt_scalef32_pk_f16_fp4 v94, v77, 1.0 op_sel:[1,0,0]
	v_cvt_scalef32_pk_f16_fp4 v97, v77, 1.0 op_sel:[0,1,0]
	v_cvt_scalef32_pk_f16_fp4 v77, v77, 1.0 op_sel:[1,1,0]
	v_pk_fma_f16 v87, v87, v63, v99
	v_pk_fma_f16 v95, v95, v63, v100
	v_pk_fma_f16 v96, v96, v63, v101
	v_pk_fma_f16 v94, v94, v63, v98
	v_pk_fma_f16 v97, v97, v63, v102
	v_pk_fma_f16 v62, v77, v63, v62
	v_mul_u32_u24_sdwa v63, v64, s93 dst_sel:DWORD dst_unused:UNUSED_PAD src0_sel:WORD_0 src1_sel:DWORD
	v_cvt_scalef32_pk_f16_fp4 v77, v70, 1.0
	v_pk_fma_f16 v77, v77, v63, v78
	v_cvt_scalef32_pk_f16_fp4 v78, v70, 1.0 op_sel:[1,0,0]
	v_pk_fma_f16 v78, v78, v63, v79
	v_cvt_scalef32_pk_f16_fp4 v79, v70, 1.0 op_sel:[0,1,0]
	v_cvt_scalef32_pk_f16_fp4 v70, v70, 1.0 op_sel:[1,1,0]
	v_pk_fma_f16 v70, v70, v63, v74
	v_cvt_scalef32_pk_f16_fp4 v74, v71, 1.0
	v_pk_fma_f16 v79, v79, v63, v87
	v_pk_fma_f16 v74, v74, v63, v84
	v_cvt_scalef32_pk_f16_fp4 v84, v71, 1.0 op_sel:[1,0,0]
	v_cvt_scalef32_pk_f16_fp4 v87, v71, 1.0 op_sel:[0,1,0]
	v_cvt_scalef32_pk_f16_fp4 v71, v71, 1.0 op_sel:[1,1,0]
	v_pk_fma_f16 v71, v71, v63, v75
	v_cvt_scalef32_pk_f16_fp4 v75, v72, 1.0
	v_pk_fma_f16 v84, v84, v63, v92
	v_pk_fma_f16 v75, v75, v63, v85
	v_cvt_scalef32_pk_f16_fp4 v85, v72, 1.0 op_sel:[1,0,0]
	v_cvt_scalef32_pk_f16_fp4 v92, v72, 1.0 op_sel:[0,1,0]
	v_cvt_scalef32_pk_f16_fp4 v72, v72, 1.0 op_sel:[1,1,0]
	v_pk_fma_f16 v72, v72, v63, v76
	v_cvt_scalef32_pk_f16_fp4 v76, v73, 1.0
	v_pk_fma_f16 v85, v85, v63, v93
	v_pk_fma_f16 v76, v76, v63, v86
	v_cvt_scalef32_pk_f16_fp4 v86, v73, 1.0 op_sel:[1,0,0]
	v_cvt_scalef32_pk_f16_fp4 v93, v73, 1.0 op_sel:[0,1,0]
	v_cvt_scalef32_pk_f16_fp4 v73, v73, 1.0 op_sel:[1,1,0]
	v_pk_fma_f16 v87, v87, v63, v95
	v_pk_fma_f16 v92, v92, v63, v96
	v_pk_fma_f16 v86, v86, v63, v94
	v_pk_fma_f16 v93, v93, v63, v97
	v_pk_fma_f16 v62, v73, v63, v62
	v_mul_u32_u24_sdwa v63, v64, s93 dst_sel:DWORD dst_unused:UNUSED_PAD src0_sel:WORD_1 src1_sel:DWORD
	v_cvt_scalef32_pk_f16_fp4 v64, v66, 1.0
	v_pk_fma_f16 v64, v64, v63, v77
	v_cvt_scalef32_pk_f16_fp4 v73, v66, 1.0 op_sel:[1,0,0]
	v_cvt_scalef32_pk_f16_fp4 v77, v66, 1.0 op_sel:[0,1,0]
	v_cvt_scalef32_pk_f16_fp4 v66, v66, 1.0 op_sel:[1,1,0]
	v_pk_fma_f16 v66, v66, v63, v70
	v_cvt_scalef32_pk_f16_fp4 v70, v67, 1.0
	v_pk_fma_f16 v73, v73, v63, v78
	v_pk_fma_f16 v70, v70, v63, v74
	v_cvt_scalef32_pk_f16_fp4 v74, v67, 1.0 op_sel:[1,0,0]
	v_cvt_scalef32_pk_f16_fp4 v78, v67, 1.0 op_sel:[0,1,0]
	v_cvt_scalef32_pk_f16_fp4 v67, v67, 1.0 op_sel:[1,1,0]
	v_pk_fma_f16 v67, v67, v63, v71
	v_cvt_scalef32_pk_f16_fp4 v71, v68, 1.0
	v_pk_fma_f16 v77, v77, v63, v79
	v_pk_fma_f16 v71, v71, v63, v75
	v_cvt_scalef32_pk_f16_fp4 v75, v68, 1.0 op_sel:[1,0,0]
	v_cvt_scalef32_pk_f16_fp4 v79, v68, 1.0 op_sel:[0,1,0]
	v_cvt_scalef32_pk_f16_fp4 v68, v68, 1.0 op_sel:[1,1,0]
	v_pk_fma_f16 v68, v68, v63, v72
	v_cvt_scalef32_pk_f16_fp4 v72, v69, 1.0
	v_pk_fma_f16 v74, v74, v63, v84
	v_pk_fma_f16 v72, v72, v63, v76
	v_cvt_scalef32_pk_f16_fp4 v76, v69, 1.0 op_sel:[1,0,0]
	v_cvt_scalef32_pk_f16_fp4 v84, v69, 1.0 op_sel:[0,1,0]
	v_cvt_scalef32_pk_f16_fp4 v69, v69, 1.0 op_sel:[1,1,0]
	v_pk_fma_f16 v78, v78, v63, v87
	v_pk_fma_f16 v75, v75, v63, v85
	v_pk_fma_f16 v79, v79, v63, v92
	v_pk_fma_f16 v76, v76, v63, v86
	v_pk_fma_f16 v84, v84, v63, v93
	v_pk_fma_f16 v62, v69, v63, v62
	v_mul_u32_u24_sdwa v63, v65, s93 dst_sel:DWORD dst_unused:UNUSED_PAD src0_sel:WORD_0 src1_sel:DWORD
	v_cvt_scalef32_pk_f16_fp4 v69, v58, 1.0
	v_pk_fma_f16 v64, v69, v63, v64
	v_cvt_scalef32_pk_f16_fp4 v69, v58, 1.0 op_sel:[1,0,0]
	v_pk_fma_f16 v69, v69, v63, v73
	v_cvt_scalef32_pk_f16_fp4 v73, v58, 1.0 op_sel:[0,1,0]
	v_cvt_scalef32_pk_f16_fp4 v58, v58, 1.0 op_sel:[1,1,0]
	v_pk_fma_f16 v58, v58, v63, v66
	v_cvt_scalef32_pk_f16_fp4 v66, v59, 1.0
	v_pk_fma_f16 v66, v66, v63, v70
	v_cvt_scalef32_pk_f16_fp4 v70, v59, 1.0 op_sel:[1,0,0]
	v_pk_fma_f16 v70, v70, v63, v74
	v_cvt_scalef32_pk_f16_fp4 v74, v59, 1.0 op_sel:[0,1,0]
	v_cvt_scalef32_pk_f16_fp4 v59, v59, 1.0 op_sel:[1,1,0]
	v_pk_fma_f16 v59, v59, v63, v67
	v_cvt_scalef32_pk_f16_fp4 v67, v60, 1.0
	v_pk_fma_f16 v67, v67, v63, v71
	v_cvt_scalef32_pk_f16_fp4 v71, v60, 1.0 op_sel:[1,0,0]
	v_pk_fma_f16 v71, v71, v63, v75
	v_cvt_scalef32_pk_f16_fp4 v75, v60, 1.0 op_sel:[0,1,0]
	v_cvt_scalef32_pk_f16_fp4 v60, v60, 1.0 op_sel:[1,1,0]
	v_pk_fma_f16 v60, v60, v63, v68
	v_cvt_scalef32_pk_f16_fp4 v68, v61, 1.0
	v_pk_fma_f16 v68, v68, v63, v72
	v_cvt_scalef32_pk_f16_fp4 v72, v61, 1.0 op_sel:[1,0,0]
	v_pk_fma_f16 v72, v72, v63, v76
	v_cvt_scalef32_pk_f16_fp4 v76, v61, 1.0 op_sel:[0,1,0]
	v_cvt_scalef32_pk_f16_fp4 v61, v61, 1.0 op_sel:[1,1,0]
	v_pk_fma_f16 v93, v61, v63, v62
	v_mul_u32_u24_sdwa v94, v65, s93 dst_sel:DWORD dst_unused:UNUSED_PAD src0_sel:WORD_1 src1_sel:DWORD
	v_cvt_scalef32_pk_f16_fp4 v61, v88, 1.0
	v_pk_fma_f16 v95, v61, v94, v64
	v_cvt_scalef32_pk_f16_fp4 v61, v88, 1.0 op_sel:[1,0,0]
	v_pk_fma_f16 v73, v73, v63, v77
	v_pk_fma_f16 v96, v61, v94, v69
	v_cvt_scalef32_pk_f16_fp4 v61, v88, 1.0 op_sel:[0,1,0]
	v_pk_fma_f16 v97, v61, v94, v73
	v_cvt_scalef32_pk_f16_fp4 v61, v88, 1.0 op_sel:[1,1,0]
	v_pk_fma_f16 v100, v61, v94, v58
	v_cvt_scalef32_pk_f16_fp4 v58, v89, 1.0
	v_pk_fma_f16 v101, v58, v94, v66
	v_cvt_scalef32_pk_f16_fp4 v58, v89, 1.0 op_sel:[1,0,0]
	v_lshlrev_b32_e32 v18, 7, v40
	v_pk_fma_f16 v74, v74, v63, v78
	v_pk_fma_f16 v104, v58, v94, v70
	v_cvt_scalef32_pk_f16_fp4 v58, v89, 1.0 op_sel:[0,1,0]
	v_and_b32_e32 v210, 0x7fff80, v18
	v_pk_fma_f16 v105, v58, v94, v74
	v_cvt_scalef32_pk_f16_fp4 v58, v89, 1.0 op_sel:[1,1,0]
	v_lshl_add_u64 v[18:19], v[116:117], 0, v[210:211]
	v_lshlrev_b32_sdwa v210, v230, v40 dst_sel:DWORD dst_unused:UNUSED_PAD src0_sel:DWORD src1_sel:WORD_1
	v_lshlrev_b32_e32 v26, 7, v41
	v_pk_fma_f16 v106, v58, v94, v59
	v_cvt_scalef32_pk_f16_fp4 v58, v90, 1.0
	v_lshl_add_u64 v[22:23], v[116:117], 0, v[210:211]
	v_and_b32_e32 v210, 0x7fff80, v26
	v_pk_fma_f16 v98, v58, v94, v67
	v_cvt_scalef32_pk_f16_fp4 v58, v90, 1.0 op_sel:[1,0,0]
	v_lshl_add_u64 v[26:27], v[116:117], 0, v[210:211]
	v_lshlrev_b32_sdwa v210, v230, v41 dst_sel:DWORD dst_unused:UNUSED_PAD src0_sel:DWORD src1_sel:WORD_1
	v_lshlrev_b32_e32 v34, 7, v42
	v_pk_fma_f16 v75, v75, v63, v79
	v_pk_fma_f16 v99, v58, v94, v71
	v_cvt_scalef32_pk_f16_fp4 v58, v90, 1.0 op_sel:[0,1,0]
	v_lshl_add_u64 v[30:31], v[116:117], 0, v[210:211]
	v_and_b32_e32 v210, 0x7fff80, v34
	v_pk_fma_f16 v102, v58, v94, v75
	v_cvt_scalef32_pk_f16_fp4 v58, v90, 1.0 op_sel:[1,1,0]
	v_lshl_add_u64 v[34:35], v[116:117], 0, v[210:211]
	v_lshlrev_b32_sdwa v210, v230, v42 dst_sel:DWORD dst_unused:UNUSED_PAD src0_sel:DWORD src1_sel:WORD_1
	v_lshlrev_b32_e32 v42, 7, v43
	v_pk_fma_f16 v103, v58, v94, v60
	v_cvt_scalef32_pk_f16_fp4 v58, v91, 1.0
	v_lshl_add_u64 v[38:39], v[116:117], 0, v[210:211]
	v_and_b32_e32 v210, 0x7fff80, v42
	v_pk_fma_f16 v107, v58, v94, v68
	v_cvt_scalef32_pk_f16_fp4 v58, v91, 1.0 op_sel:[1,0,0]
	v_lshl_add_u64 v[44:45], v[116:117], 0, v[210:211]
	v_lshlrev_b32_sdwa v210, v230, v43 dst_sel:DWORD dst_unused:UNUSED_PAD src0_sel:DWORD src1_sel:WORD_1
	v_pk_fma_f16 v108, v58, v94, v72
	v_lshlrev_b32_e32 v58, 7, v80
	v_lshl_add_u64 v[46:47], v[116:117], 0, v[210:211]
	v_and_b32_e32 v210, 0x7fff80, v58
	v_lshl_add_u64 v[58:59], v[116:117], 0, v[210:211]
	v_lshlrev_b32_sdwa v210, v230, v80 dst_sel:DWORD dst_unused:UNUSED_PAD src0_sel:DWORD src1_sel:WORD_1
	v_lshlrev_b32_e32 v66, 7, v81
	v_pk_fma_f16 v92, v76, v63, v84
	v_lshl_add_u64 v[62:63], v[116:117], 0, v[210:211]
	v_and_b32_e32 v210, 0x7fff80, v66
	v_lshl_add_u64 v[66:67], v[116:117], 0, v[210:211]
	v_lshlrev_b32_sdwa v210, v230, v81 dst_sel:DWORD dst_unused:UNUSED_PAD src0_sel:DWORD src1_sel:WORD_1
	v_lshlrev_b32_e32 v74, 7, v82
	v_lshl_add_u64 v[70:71], v[116:117], 0, v[210:211]
	v_and_b32_e32 v210, 0x7fff80, v74
	v_lshl_add_u64 v[74:75], v[116:117], 0, v[210:211]
	v_lshlrev_b32_sdwa v210, v230, v82 dst_sel:DWORD dst_unused:UNUSED_PAD src0_sel:DWORD src1_sel:WORD_1
	v_lshlrev_b32_e32 v82, 7, v83
	v_lshl_add_u64 v[78:79], v[116:117], 0, v[210:211]
	v_and_b32_e32 v210, 0x7fff80, v82
	v_lshl_add_u64 v[84:85], v[116:117], 0, v[210:211]
	v_lshlrev_b32_sdwa v210, v230, v83 dst_sel:DWORD dst_unused:UNUSED_PAD src0_sel:DWORD src1_sel:WORD_1
	v_lshl_add_u64 v[86:87], v[116:117], 0, v[210:211]
	v_cvt_scalef32_pk_f16_fp4 v90, v91, 1.0 op_sel:[0,1,0]
	v_pk_fma_f16 v109, v90, v94, v92
	v_cvt_scalef32_pk_f16_fp4 v90, v91, 1.0 op_sel:[1,1,0]
	v_permlane32_swap_b32_e32 v96, v99
	v_pk_fma_f16 v110, v90, v94, v93
	v_permlane32_swap_b32_e32 v95, v98
	v_pk_add_f16 v92, v96, v99
	v_permlane32_swap_b32_e32 v97, v102
	v_pk_add_f16 v91, v95, v98
	v_cvt_f32_f16_e32 v98, v92
	v_cvt_f32_f16_sdwa v99, v92 dst_sel:DWORD dst_unused:UNUSED_PAD src0_sel:WORD_1
	v_pk_add_f16 v92, v97, v102
	v_permlane32_swap_b32_e32 v100, v103
	v_permlane32_swap_b32_e32 v101, v107
	v_permlane32_swap_b32_e32 v104, v108
	v_permlane32_swap_b32_e32 v105, v109
	v_permlane32_swap_b32_e32 v106, v110
	v_cvt_f32_f16_e32 v94, v92
	v_cvt_f32_f16_sdwa v95, v92 dst_sel:DWORD dst_unused:UNUSED_PAD src0_sel:WORD_1
	v_pk_add_f16 v92, v100, v103
	v_pk_add_f16 v93, v101, v107
	v_pk_add_f16 v96, v104, v108
	v_pk_add_f16 v97, v105, v109
	v_pk_add_f16 v105, v106, v110
	v_cvt_f32_f16_e32 v90, v91
	v_cvt_f32_f16_sdwa v91, v91 dst_sel:DWORD dst_unused:UNUSED_PAD src0_sel:WORD_1
	v_cvt_f32_f16_e32 v102, v92
	v_cvt_f32_f16_sdwa v103, v92 dst_sel:DWORD dst_unused:UNUSED_PAD src0_sel:WORD_1
	v_cvt_f32_f16_e32 v92, v93
	v_cvt_f32_f16_sdwa v93, v93 dst_sel:DWORD dst_unused:UNUSED_PAD src0_sel:WORD_1
	v_cvt_f32_f16_e32 v100, v96
	v_cvt_f32_f16_sdwa v101, v96 dst_sel:DWORD dst_unused:UNUSED_PAD src0_sel:WORD_1
	v_cvt_f32_f16_e32 v96, v97
	v_cvt_f32_f16_sdwa v97, v97 dst_sel:DWORD dst_unused:UNUSED_PAD src0_sel:WORD_1
	v_cvt_f32_f16_e32 v104, v105
	v_cvt_f32_f16_sdwa v105, v105 dst_sel:DWORD dst_unused:UNUSED_PAD src0_sel:WORD_1
	v_mul_hi_i32 v106, v113, s69
	v_lshrrev_b32_e32 v107, 31, v106
	v_ashrrev_i32_e32 v106, 13, v106
	v_add_u32_e32 v107, v106, v107
	v_permlane16_swap_b32_e32 v90, v92
	v_permlane16_swap_b32_e32 v91, v93
	v_permlane16_swap_b32_e32 v98, v100
	v_permlane16_swap_b32_e32 v99, v101
	v_permlane16_swap_b32_e32 v94, v96
	v_permlane16_swap_b32_e32 v95, v97
	v_permlane16_swap_b32_e32 v102, v104
	v_permlane16_swap_b32_e32 v103, v105
	v_mul_i32_i24_e32 v110, 0xffffbf00, v107
	v_pk_add_f32 v[92:93], v[90:91], v[92:93]
	v_pk_add_f32 v[90:91], v[94:95], v[96:97]
	v_pk_add_f32 v[100:101], v[98:99], v[100:101]
	v_pk_add_f32 v[98:99], v[102:103], v[104:105]
	v_add3_u32 v106, v112, v110, s33
	v_mov_b32_dpp v96, v92 row_ror:8 row_mask:0xf bank_mask:0xf bound_ctrl:1
	v_mov_b32_dpp v94, v90 row_ror:8 row_mask:0xf bank_mask:0xf bound_ctrl:1
	v_mov_b32_dpp v97, v93 row_ror:8 row_mask:0xf bank_mask:0xf bound_ctrl:1
	v_mov_b32_dpp v95, v91 row_ror:8 row_mask:0xf bank_mask:0xf bound_ctrl:1
	v_mov_b32_dpp v104, v100 row_ror:8 row_mask:0xf bank_mask:0xf bound_ctrl:1
	v_mov_b32_dpp v102, v98 row_ror:8 row_mask:0xf bank_mask:0xf bound_ctrl:1
	v_mov_b32_dpp v105, v101 row_ror:8 row_mask:0xf bank_mask:0xf bound_ctrl:1
	v_mov_b32_dpp v103, v99 row_ror:8 row_mask:0xf bank_mask:0xf bound_ctrl:1
	v_cmp_gt_i32_e32 vcc, s68, v106
	v_cmp_lt_i32_e64 s[0:1], s21, v106
	s_and_saveexec_b64 s[2:3], s[0:1]
	s_xor_b64 s[0:1], exec, s[2:3]
	v_lshl_add_u32 v106, v107, 14, v110
	v_add3_u32 v106, v113, v106, s88
	s_or_saveexec_b64 s[0:1], s[0:1]
	v_mov_b64_e32 v[108:109], s[18:19]
	s_xor_b64 exec, exec, s[0:1]
	v_lshlrev_b32_e32 v106, 8, v107
	v_add3_u32 v106, v110, v113, v106
	v_mov_b64_e32 v[108:109], s[72:73]
	s_or_b64 exec, exec, s[0:1]
	v_mul_i32_i24_e32 v107, 0x3000, v107
	v_cndmask_b32_e32 v110, v107, v223, vcc
	v_ashrrev_i32_e32 v111, 31, v110
	v_lshl_add_u64 v[110:111], v[110:111], 2, s[10:11]
	v_lshlrev_b32_e32 v210, 2, v118
	v_ashrrev_i32_e32 v107, 31, v106
	v_lshl_add_u64 v[122:123], v[110:111], 0, v[210:211]
	v_lshlrev_b64 v[106:107], 13, v[106:107]
	v_lshl_add_u64 v[106:107], v[108:109], 0, v[106:107]
	v_add_co_u32_e32 v122, vcc, s94, v122
	v_lshl_add_u64 v[126:127], v[106:107], 0, v[210:211]
	s_nop 0
	v_addc_co_u32_e32 v123, vcc, 0, v123, vcc
	v_pk_add_f32 v[92:93], v[92:93], v[96:97]
	v_pk_add_f32 v[96:97], v[100:101], v[104:105]
	v_pk_add_f32 v[90:91], v[90:91], v[94:95]
	v_pk_add_f32 v[94:95], v[98:99], v[102:103]
	v_cndmask_b32_e64 v91, v91, v93, s[38:39]
	v_cndmask_b32_e64 v95, v95, v97, s[38:39]
	v_cndmask_b32_e64 v94, v94, v96, s[38:39]
	v_cndmask_b32_e64 v90, v90, v92, s[38:39]
	s_waitcnt vmcnt(2)
	v_mul_u32_u24_sdwa v98, v50, s93 dst_sel:DWORD dst_unused:UNUSED_PAD src0_sel:WORD_0 src1_sel:DWORD
	v_mul_u32_u24_sdwa v97, v50, s93 dst_sel:DWORD dst_unused:UNUSED_PAD src0_sel:WORD_1 src1_sel:DWORD
	v_mul_u32_u24_sdwa v96, v51, s93 dst_sel:DWORD dst_unused:UNUSED_PAD src0_sel:WORD_1 src1_sel:DWORD
	v_mul_u32_u24_sdwa v51, v51, s93 dst_sel:DWORD dst_unused:UNUSED_PAD src0_sel:WORD_0 src1_sel:DWORD
	s_waitcnt vmcnt(2)
	v_cvt_scalef32_pk_f16_fp4 v119, v143, 1.0 op_sel:[1,1,0]
	s_waitcnt vmcnt(2)
	v_cvt_scalef32_pk_f16_fp4 v111, v147, 1.0 op_sel:[1,1,0]
	s_waitcnt vmcnt(2)
	v_cvt_scalef32_pk_f16_fp4 v105, v167, 1.0 op_sel:[1,1,0]
	s_waitcnt vmcnt(2)
	v_cvt_scalef32_pk_f16_fp4 v104, v171, 1.0 op_sel:[1,1,0]
	s_waitcnt vmcnt(2)
	v_cvt_scalef32_pk_f16_fp4 v103, v175, 1.0 op_sel:[1,1,0]
	s_waitcnt vmcnt(2)
	v_cvt_scalef32_pk_f16_fp4 v102, v179, 1.0 op_sel:[1,1,0]
	s_waitcnt vmcnt(2)
	v_cvt_scalef32_pk_f16_fp4 v101, v183, 1.0 op_sel:[1,1,0]
	s_waitcnt vmcnt(2)
	v_cvt_scalef32_pk_f16_fp4 v100, v187, 1.0 op_sel:[1,1,0]
	s_waitcnt vmcnt(2)
	v_cvt_scalef32_pk_f16_fp4 v99, v191, 1.0 op_sel:[1,1,0]
	v_add_u32_e32 v110, 1, v113
	s_waitcnt vmcnt(0)
	v_pk_fma_f32 v[92:93], v[202:203], v[94:95], v[198:199]
	v_cvt_scalef32_pk_f16_fp4 v124, v131, 1.0 op_sel:[1,1,0]
	v_pk_fma_f32 v[90:91], v[200:201], v[90:91], v[196:197]
	v_cvt_scalef32_pk_f16_fp4 v123, v135, 1.0 op_sel:[1,1,0]
	v_pk_fma_f16 v50, v124, v98, 0
	v_cvt_scalef32_pk_f16_fp4 v124, v131, 1.0 op_sel:[0,1,0]
	v_cvt_scalef32_pk_f16_fp4 v122, v139, 1.0 op_sel:[1,1,0]
	v_pk_fma_f16 v50, v123, v97, v50
	v_cvt_scalef32_pk_f16_fp4 v123, v135, 1.0 op_sel:[0,1,0]
	v_pk_fma_f16 v124, v124, v98, 0
	v_cvt_scalef32_pk_f16_fp4 v125, v131, 1.0 op_sel:[1,0,0]
	v_pk_fma_f16 v50, v122, v51, v50
	v_cvt_scalef32_pk_f16_fp4 v122, v139, 1.0 op_sel:[0,1,0]
	v_pk_fma_f16 v123, v123, v97, v124
	v_cvt_scalef32_pk_f16_fp4 v124, v135, 1.0 op_sel:[1,0,0]
	v_pk_fma_f16 v125, v125, v98, 0
	v_cvt_scalef32_pk_f16_fp4 v21, v131, 1.0
	v_mul_u32_u24_sdwa v95, v52, s93 dst_sel:DWORD dst_unused:UNUSED_PAD src0_sel:WORD_1 src1_sel:DWORD
	v_mul_u32_u24_sdwa v52, v52, s93 dst_sel:DWORD dst_unused:UNUSED_PAD src0_sel:WORD_0 src1_sel:DWORD
	v_pk_fma_f16 v50, v119, v96, v50
	v_cvt_scalef32_pk_f16_fp4 v119, v143, 1.0 op_sel:[0,1,0]
	v_pk_fma_f16 v122, v122, v51, v123
	v_cvt_scalef32_pk_f16_fp4 v123, v139, 1.0 op_sel:[1,0,0]
	v_pk_fma_f16 v124, v124, v97, v125
	v_cvt_scalef32_pk_f16_fp4 v25, v135, 1.0
	v_pk_fma_f16 v21, v21, v98, 0
	v_cvt_scalef32_pk_f16_fp4 v109, v151, 1.0 op_sel:[1,1,0]
	v_pk_fma_f16 v50, v111, v52, v50
	v_cvt_scalef32_pk_f16_fp4 v111, v147, 1.0 op_sel:[0,1,0]
	v_pk_fma_f16 v119, v119, v96, v122
	v_cvt_scalef32_pk_f16_fp4 v122, v143, 1.0 op_sel:[1,0,0]
	v_pk_fma_f16 v123, v123, v51, v124
	v_cvt_scalef32_pk_f16_fp4 v29, v139, 1.0
	v_pk_fma_f16 v21, v25, v97, v21
	v_mul_u32_u24_sdwa v94, v53, s93 dst_sel:DWORD dst_unused:UNUSED_PAD src0_sel:WORD_1 src1_sel:DWORD
	v_cvt_scalef32_pk_f16_fp4 v108, v155, 1.0 op_sel:[1,1,0]
	v_mul_u32_u24_sdwa v53, v53, s93 dst_sel:DWORD dst_unused:UNUSED_PAD src0_sel:WORD_0 src1_sel:DWORD
	v_pk_fma_f16 v50, v109, v95, v50
	v_cvt_scalef32_pk_f16_fp4 v109, v151, 1.0 op_sel:[0,1,0]
	v_pk_fma_f16 v111, v111, v52, v119
	v_cvt_scalef32_pk_f16_fp4 v119, v147, 1.0 op_sel:[1,0,0]
	v_pk_fma_f16 v122, v122, v96, v123
	v_cvt_scalef32_pk_f16_fp4 v33, v143, 1.0
	v_pk_fma_f16 v21, v29, v51, v21
	v_cvt_scalef32_pk_f16_fp4 v107, v159, 1.0 op_sel:[1,1,0]
	v_pk_fma_f16 v50, v108, v53, v50
	v_cvt_scalef32_pk_f16_fp4 v108, v155, 1.0 op_sel:[0,1,0]
	v_pk_fma_f16 v109, v109, v95, v111
	v_cvt_scalef32_pk_f16_fp4 v111, v151, 1.0 op_sel:[1,0,0]
	v_pk_fma_f16 v119, v119, v52, v122
	v_cvt_scalef32_pk_f16_fp4 v37, v147, 1.0
	v_pk_fma_f16 v21, v33, v96, v21
	global_store_dwordx4 v[126:127], v[90:93], off
	v_add_u32_e32 v218, 1, v113
	v_mul_hi_i32 v244, v218, s69
	v_lshrrev_b32_e32 v245, 31, v244
	v_ashrrev_i32_e32 v244, 13, v244
	v_add_u32_e32 v245, v244, v245
	v_mul_i32_i24_e32 v248, 0xffffbf00, v245
	v_add_u32_e32 v244, v218, v248
	v_cmp_gt_i32_e32 vcc, s68, v244
	v_cmp_lt_i32_e64 s[0:1], s21, v244
	s_and_saveexec_b64 s[2:3], s[0:1]
	s_xor_b64 s[0:1], exec, s[2:3]
	v_lshl_add_u32 v244, v245, 14, v248
	v_add3_u32 v244, v218, v244, s88
	s_or_saveexec_b64 s[0:1], s[0:1]
	v_mov_b64_e32 v[246:247], s[18:19]
	s_xor_b64 exec, exec, s[0:1]
	v_lshlrev_b32_e32 v244, 8, v245
	v_add3_u32 v244, v248, v218, v244
	v_mov_b64_e32 v[246:247], s[72:73]
	s_or_b64 exec, exec, s[0:1]
	v_mul_i32_i24_e32 v245, 0x3000, v245
	v_cndmask_b32_e32 v248, v245, v223, vcc
	v_ashrrev_i32_e32 v249, 31, v248
	v_lshl_add_u64 v[248:249], v[248:249], 2, s[10:11]
	v_lshlrev_b32_e32 v210, 2, v118
	v_ashrrev_i32_e32 v245, 31, v244
	v_lshl_add_u64 v[250:251], v[248:249], 0, v[210:211]
	v_lshlrev_b64 v[244:245], 13, v[244:245]
	v_lshl_add_u64 v[244:245], v[246:247], 0, v[244:245]
	v_add_co_u32_e32 v250, vcc, s94, v250
	v_lshl_add_u64 v[204:205], v[244:245], 0, v[210:211]
	s_nop 0
	v_addc_co_u32_e32 v251, vcc, 0, v251, vcc
	global_load_dwordx4 v[234:237], v[204:205], off
	global_load_dwordx4 v[238:241], v[250:251], off
	v_cvt_scalef32_pk_f16_fp4 v106, v163, 1.0 op_sel:[1,1,0]
	v_pk_fma_f16 v50, v107, v94, v50
	v_mul_u32_u24_sdwa v93, v54, s93 dst_sel:DWORD dst_unused:UNUSED_PAD src0_sel:WORD_1 src1_sel:DWORD
	v_mul_u32_u24_sdwa v54, v54, s93 dst_sel:DWORD dst_unused:UNUSED_PAD src0_sel:WORD_0 src1_sel:DWORD
	v_cvt_scalef32_pk_f16_fp4 v107, v159, 1.0 op_sel:[0,1,0]
	v_pk_fma_f16 v108, v108, v53, v109
	v_cvt_scalef32_pk_f16_fp4 v109, v155, 1.0 op_sel:[1,0,0]
	v_pk_fma_f16 v111, v111, v95, v119
	v_cvt_scalef32_pk_f16_fp4 v41, v151, 1.0
	v_pk_fma_f16 v21, v37, v52, v21
	v_pk_fma_f16 v50, v106, v54, v50
	v_cvt_scalef32_pk_f16_fp4 v106, v163, 1.0 op_sel:[0,1,0]
	v_pk_fma_f16 v107, v107, v94, v108
	v_cvt_scalef32_pk_f16_fp4 v108, v159, 1.0 op_sel:[1,0,0]
	v_pk_fma_f16 v109, v109, v53, v111
	v_cvt_scalef32_pk_f16_fp4 v45, v155, 1.0
	v_pk_fma_f16 v21, v41, v95, v21
	v_mul_u32_u24_sdwa v92, v55, s93 dst_sel:DWORD dst_unused:UNUSED_PAD src0_sel:WORD_1 src1_sel:DWORD
	v_mul_u32_u24_sdwa v55, v55, s93 dst_sel:DWORD dst_unused:UNUSED_PAD src0_sel:WORD_0 src1_sel:DWORD
	v_pk_fma_f16 v50, v105, v93, v50
	v_cvt_scalef32_pk_f16_fp4 v105, v167, 1.0 op_sel:[0,1,0]
	v_pk_fma_f16 v106, v106, v54, v107
	v_cvt_scalef32_pk_f16_fp4 v107, v163, 1.0 op_sel:[1,0,0]
	v_pk_fma_f16 v108, v108, v94, v109
	v_cvt_scalef32_pk_f16_fp4 v49, v159, 1.0
	v_pk_fma_f16 v21, v45, v53, v21
	v_pk_fma_f16 v50, v104, v55, v50
	v_cvt_scalef32_pk_f16_fp4 v104, v171, 1.0 op_sel:[0,1,0]
	v_pk_fma_f16 v105, v105, v93, v106
	v_cvt_scalef32_pk_f16_fp4 v106, v167, 1.0 op_sel:[1,0,0]
	v_pk_fma_f16 v107, v107, v54, v108
	v_cvt_scalef32_pk_f16_fp4 v61, v163, 1.0
	v_pk_fma_f16 v21, v49, v94, v21
	v_mul_u32_u24_sdwa v91, v56, s93 dst_sel:DWORD dst_unused:UNUSED_PAD src0_sel:WORD_1 src1_sel:DWORD
	v_mul_u32_u24_sdwa v56, v56, s93 dst_sel:DWORD dst_unused:UNUSED_PAD src0_sel:WORD_0 src1_sel:DWORD
	v_pk_fma_f16 v50, v103, v92, v50
	v_cvt_scalef32_pk_f16_fp4 v103, v175, 1.0 op_sel:[0,1,0]
	v_pk_fma_f16 v104, v104, v55, v105
	v_cvt_scalef32_pk_f16_fp4 v105, v171, 1.0 op_sel:[1,0,0]
	v_pk_fma_f16 v106, v106, v93, v107
	v_cvt_scalef32_pk_f16_fp4 v65, v167, 1.0
	v_pk_fma_f16 v21, v61, v54, v21
	v_pk_fma_f16 v50, v102, v56, v50
	v_cvt_scalef32_pk_f16_fp4 v102, v179, 1.0 op_sel:[0,1,0]
	v_pk_fma_f16 v103, v103, v92, v104
	v_cvt_scalef32_pk_f16_fp4 v104, v175, 1.0 op_sel:[1,0,0]
	v_pk_fma_f16 v105, v105, v55, v106
	v_cvt_scalef32_pk_f16_fp4 v69, v171, 1.0
	v_pk_fma_f16 v21, v65, v93, v21
	v_mul_u32_u24_sdwa v90, v57, s93 dst_sel:DWORD dst_unused:UNUSED_PAD src0_sel:WORD_1 src1_sel:DWORD
	v_mul_u32_u24_sdwa v57, v57, s93 dst_sel:DWORD dst_unused:UNUSED_PAD src0_sel:WORD_0 src1_sel:DWORD
	v_pk_fma_f16 v50, v101, v91, v50
	v_cvt_scalef32_pk_f16_fp4 v101, v183, 1.0 op_sel:[0,1,0]
	v_pk_fma_f16 v102, v102, v56, v103
	v_cvt_scalef32_pk_f16_fp4 v103, v179, 1.0 op_sel:[1,0,0]
	v_pk_fma_f16 v104, v104, v92, v105
	v_cvt_scalef32_pk_f16_fp4 v73, v175, 1.0
	v_pk_fma_f16 v21, v69, v55, v21
	v_pk_fma_f16 v50, v100, v57, v50
	v_cvt_scalef32_pk_f16_fp4 v100, v187, 1.0 op_sel:[0,1,0]
	v_pk_fma_f16 v101, v101, v91, v102
	v_cvt_scalef32_pk_f16_fp4 v102, v183, 1.0 op_sel:[1,0,0]
	v_pk_fma_f16 v103, v103, v56, v104
	v_cvt_scalef32_pk_f16_fp4 v77, v179, 1.0
	v_pk_fma_f16 v21, v73, v92, v21
	v_pk_fma_f16 v50, v99, v90, v50
	v_cvt_scalef32_pk_f16_fp4 v99, v191, 1.0 op_sel:[0,1,0]
	v_pk_fma_f16 v100, v100, v57, v101
	v_cvt_scalef32_pk_f16_fp4 v101, v187, 1.0 op_sel:[1,0,0]
	v_pk_fma_f16 v102, v102, v91, v103
	v_cvt_scalef32_pk_f16_fp4 v81, v183, 1.0
	v_pk_fma_f16 v21, v77, v56, v21
	v_pk_fma_f16 v99, v99, v90, v100
	v_cvt_scalef32_pk_f16_fp4 v100, v191, 1.0 op_sel:[1,0,0]
	v_pk_fma_f16 v101, v101, v57, v102
	v_cvt_scalef32_pk_f16_fp4 v85, v187, 1.0
	v_pk_fma_f16 v21, v81, v91, v21
	v_pk_fma_f16 v100, v100, v90, v101
	v_cvt_scalef32_pk_f16_fp4 v89, v191, 1.0
	v_pk_fma_f16 v21, v85, v57, v21
	v_cvt_scalef32_pk_f16_fp4 v101, v130, 1.0 op_sel:[1,1,0]
	v_pk_fma_f16 v21, v89, v90, v21
	v_cvt_scalef32_pk_f16_fp4 v89, v134, 1.0 op_sel:[1,1,0]
	v_pk_fma_f16 v101, v101, v98, 0
	v_cvt_scalef32_pk_f16_fp4 v102, v130, 1.0 op_sel:[0,1,0]
	v_cvt_scalef32_pk_f16_fp4 v85, v138, 1.0 op_sel:[1,1,0]
	v_pk_fma_f16 v89, v89, v97, v101
	v_cvt_scalef32_pk_f16_fp4 v101, v134, 1.0 op_sel:[0,1,0]
	v_pk_fma_f16 v102, v102, v98, 0
	v_cvt_scalef32_pk_f16_fp4 v103, v130, 1.0 op_sel:[1,0,0]
	v_cvt_scalef32_pk_f16_fp4 v81, v142, 1.0 op_sel:[1,1,0]
	v_pk_fma_f16 v85, v85, v51, v89
	v_cvt_scalef32_pk_f16_fp4 v89, v138, 1.0 op_sel:[0,1,0]
	v_pk_fma_f16 v101, v101, v97, v102
	v_cvt_scalef32_pk_f16_fp4 v102, v134, 1.0 op_sel:[1,0,0]
	v_pk_fma_f16 v103, v103, v98, 0
	v_cvt_scalef32_pk_f16_fp4 v20, v130, 1.0
	v_cvt_scalef32_pk_f16_fp4 v77, v146, 1.0 op_sel:[1,1,0]
	v_pk_fma_f16 v81, v81, v96, v85
	v_cvt_scalef32_pk_f16_fp4 v85, v142, 1.0 op_sel:[0,1,0]
	v_pk_fma_f16 v89, v89, v51, v101
	v_cvt_scalef32_pk_f16_fp4 v101, v138, 1.0 op_sel:[1,0,0]
	v_pk_fma_f16 v102, v102, v97, v103
	v_cvt_scalef32_pk_f16_fp4 v24, v134, 1.0
	v_pk_fma_f16 v20, v20, v98, 0
	v_cvt_scalef32_pk_f16_fp4 v73, v150, 1.0 op_sel:[1,1,0]
	v_pk_fma_f16 v77, v77, v52, v81
	v_cvt_scalef32_pk_f16_fp4 v81, v146, 1.0 op_sel:[0,1,0]
	v_pk_fma_f16 v85, v85, v96, v89
	v_cvt_scalef32_pk_f16_fp4 v89, v142, 1.0 op_sel:[1,0,0]
	v_pk_fma_f16 v101, v101, v51, v102
	v_cvt_scalef32_pk_f16_fp4 v28, v138, 1.0
	v_pk_fma_f16 v20, v24, v97, v20
	v_cvt_scalef32_pk_f16_fp4 v69, v154, 1.0 op_sel:[1,1,0]
	v_pk_fma_f16 v73, v73, v95, v77
	v_cvt_scalef32_pk_f16_fp4 v77, v150, 1.0 op_sel:[0,1,0]
	v_pk_fma_f16 v81, v81, v52, v85
	v_cvt_scalef32_pk_f16_fp4 v85, v146, 1.0 op_sel:[1,0,0]
	v_pk_fma_f16 v89, v89, v96, v101
	v_cvt_scalef32_pk_f16_fp4 v32, v142, 1.0
	v_pk_fma_f16 v20, v28, v51, v20
	v_cvt_scalef32_pk_f16_fp4 v65, v158, 1.0 op_sel:[1,1,0]
	v_pk_fma_f16 v69, v69, v53, v73
	v_cvt_scalef32_pk_f16_fp4 v73, v154, 1.0 op_sel:[0,1,0]
	v_pk_fma_f16 v77, v77, v95, v81
	v_cvt_scalef32_pk_f16_fp4 v81, v150, 1.0 op_sel:[1,0,0]
	v_pk_fma_f16 v85, v85, v52, v89
	v_cvt_scalef32_pk_f16_fp4 v36, v146, 1.0
	v_pk_fma_f16 v20, v32, v96, v20
	v_cvt_scalef32_pk_f16_fp4 v61, v162, 1.0 op_sel:[1,1,0]
	v_pk_fma_f16 v65, v65, v94, v69
	v_cvt_scalef32_pk_f16_fp4 v69, v158, 1.0 op_sel:[0,1,0]
	v_pk_fma_f16 v73, v73, v53, v77
	v_cvt_scalef32_pk_f16_fp4 v77, v154, 1.0 op_sel:[1,0,0]
	v_pk_fma_f16 v81, v81, v95, v85
	v_cvt_scalef32_pk_f16_fp4 v40, v150, 1.0
	v_pk_fma_f16 v20, v36, v52, v20
	v_cvt_scalef32_pk_f16_fp4 v49, v166, 1.0 op_sel:[1,1,0]
	v_pk_fma_f16 v61, v61, v54, v65
	v_cvt_scalef32_pk_f16_fp4 v65, v162, 1.0 op_sel:[0,1,0]
	v_pk_fma_f16 v69, v69, v94, v73
	v_cvt_scalef32_pk_f16_fp4 v73, v158, 1.0 op_sel:[1,0,0]
	v_pk_fma_f16 v77, v77, v53, v81
	v_cvt_scalef32_pk_f16_fp4 v44, v154, 1.0
	v_pk_fma_f16 v20, v40, v95, v20
	v_cvt_scalef32_pk_f16_fp4 v45, v170, 1.0 op_sel:[1,1,0]
	v_pk_fma_f16 v49, v49, v93, v61
	v_cvt_scalef32_pk_f16_fp4 v61, v166, 1.0 op_sel:[0,1,0]
	v_pk_fma_f16 v65, v65, v54, v69
	v_cvt_scalef32_pk_f16_fp4 v69, v162, 1.0 op_sel:[1,0,0]
	v_pk_fma_f16 v73, v73, v94, v77
	v_cvt_scalef32_pk_f16_fp4 v48, v158, 1.0
	v_pk_fma_f16 v20, v44, v53, v20
	v_pk_fma_f16 v45, v45, v55, v49
	v_cvt_scalef32_pk_f16_fp4 v49, v170, 1.0 op_sel:[0,1,0]
	v_pk_fma_f16 v61, v61, v93, v65
	v_cvt_scalef32_pk_f16_fp4 v65, v166, 1.0 op_sel:[1,0,0]
	v_pk_fma_f16 v69, v69, v54, v73
	v_cvt_scalef32_pk_f16_fp4 v60, v162, 1.0
	v_pk_fma_f16 v20, v48, v94, v20
	v_cvt_scalef32_pk_f16_fp4 v41, v174, 1.0 op_sel:[1,1,0]
	v_pk_fma_f16 v49, v49, v55, v61
	v_cvt_scalef32_pk_f16_fp4 v61, v170, 1.0 op_sel:[1,0,0]
	v_pk_fma_f16 v65, v65, v93, v69
	v_cvt_scalef32_pk_f16_fp4 v64, v166, 1.0
	v_pk_fma_f16 v20, v60, v54, v20
	v_pk_fma_f16 v41, v41, v92, v45
	v_cvt_scalef32_pk_f16_fp4 v45, v174, 1.0 op_sel:[0,1,0]
	v_pk_fma_f16 v61, v61, v55, v65
	v_cvt_scalef32_pk_f16_fp4 v65, v170, 1.0
	v_pk_fma_f16 v20, v64, v93, v20
	v_cvt_scalef32_pk_f16_fp4 v68, v129, 1.0 op_sel:[1,1,0]
	v_cvt_scalef32_pk_f16_fp4 v37, v178, 1.0 op_sel:[1,1,0]
	v_pk_fma_f16 v45, v45, v92, v49
	v_cvt_scalef32_pk_f16_fp4 v49, v174, 1.0 op_sel:[1,0,0]
	v_pk_fma_f16 v20, v65, v55, v20
	v_cvt_scalef32_pk_f16_fp4 v65, v133, 1.0 op_sel:[1,1,0]
	v_pk_fma_f16 v68, v68, v98, 0
	v_cvt_scalef32_pk_f16_fp4 v69, v129, 1.0 op_sel:[0,1,0]
	v_pk_fma_f16 v37, v37, v56, v41
	v_cvt_scalef32_pk_f16_fp4 v41, v178, 1.0 op_sel:[0,1,0]
	v_pk_fma_f16 v49, v49, v92, v61
	v_cvt_scalef32_pk_f16_fp4 v61, v174, 1.0
	v_cvt_scalef32_pk_f16_fp4 v64, v137, 1.0 op_sel:[1,1,0]
	v_pk_fma_f16 v65, v65, v97, v68
	v_cvt_scalef32_pk_f16_fp4 v68, v133, 1.0 op_sel:[0,1,0]
	v_pk_fma_f16 v69, v69, v98, 0
	v_cvt_scalef32_pk_f16_fp4 v72, v129, 1.0 op_sel:[1,0,0]
	v_cvt_scalef32_pk_f16_fp4 v33, v182, 1.0 op_sel:[1,1,0]
	v_pk_fma_f16 v41, v41, v56, v45
	v_cvt_scalef32_pk_f16_fp4 v45, v178, 1.0 op_sel:[1,0,0]
	v_pk_fma_f16 v20, v61, v92, v20
	v_cvt_scalef32_pk_f16_fp4 v61, v141, 1.0 op_sel:[1,1,0]
	v_pk_fma_f16 v64, v64, v51, v65
	v_cvt_scalef32_pk_f16_fp4 v65, v137, 1.0 op_sel:[0,1,0]
	v_pk_fma_f16 v68, v68, v97, v69
	v_cvt_scalef32_pk_f16_fp4 v69, v133, 1.0 op_sel:[1,0,0]
	v_pk_fma_f16 v72, v72, v98, 0
	v_cvt_scalef32_pk_f16_fp4 v19, v129, 1.0
	v_pk_fma_f16 v33, v33, v91, v37
	v_cvt_scalef32_pk_f16_fp4 v37, v182, 1.0 op_sel:[0,1,0]
	v_pk_fma_f16 v45, v45, v56, v49
	v_cvt_scalef32_pk_f16_fp4 v49, v178, 1.0
	v_cvt_scalef32_pk_f16_fp4 v60, v145, 1.0 op_sel:[1,1,0]
	v_pk_fma_f16 v61, v61, v96, v64
	v_cvt_scalef32_pk_f16_fp4 v64, v141, 1.0 op_sel:[0,1,0]
	v_pk_fma_f16 v65, v65, v51, v68
	v_cvt_scalef32_pk_f16_fp4 v68, v137, 1.0 op_sel:[1,0,0]
	v_pk_fma_f16 v69, v69, v97, v72
	v_cvt_scalef32_pk_f16_fp4 v23, v133, 1.0
	v_pk_fma_f16 v19, v19, v98, 0
	v_cvt_scalef32_pk_f16_fp4 v29, v186, 1.0 op_sel:[1,1,0]
	v_pk_fma_f16 v37, v37, v91, v41
	v_cvt_scalef32_pk_f16_fp4 v41, v182, 1.0 op_sel:[1,0,0]
	v_pk_fma_f16 v20, v49, v56, v20
	v_cvt_scalef32_pk_f16_fp4 v49, v149, 1.0 op_sel:[1,1,0]
	v_pk_fma_f16 v60, v60, v52, v61
	v_cvt_scalef32_pk_f16_fp4 v61, v145, 1.0 op_sel:[0,1,0]
	v_pk_fma_f16 v64, v64, v96, v65
	v_cvt_scalef32_pk_f16_fp4 v65, v141, 1.0 op_sel:[1,0,0]
	v_pk_fma_f16 v68, v68, v51, v69
	v_cvt_scalef32_pk_f16_fp4 v27, v137, 1.0
	v_pk_fma_f16 v19, v23, v97, v19
	v_pk_fma_f16 v29, v29, v57, v33
	v_cvt_scalef32_pk_f16_fp4 v33, v186, 1.0 op_sel:[0,1,0]
	v_pk_fma_f16 v41, v41, v91, v45
	v_cvt_scalef32_pk_f16_fp4 v45, v182, 1.0
	v_cvt_scalef32_pk_f16_fp4 v48, v153, 1.0 op_sel:[1,1,0]
	v_pk_fma_f16 v49, v49, v95, v60
	v_cvt_scalef32_pk_f16_fp4 v60, v149, 1.0 op_sel:[0,1,0]
	v_pk_fma_f16 v61, v61, v52, v64
	v_cvt_scalef32_pk_f16_fp4 v64, v145, 1.0 op_sel:[1,0,0]
	v_pk_fma_f16 v65, v65, v96, v68
	v_cvt_scalef32_pk_f16_fp4 v31, v141, 1.0
	v_pk_fma_f16 v19, v27, v51, v19
	v_pk_fma_f16 v33, v33, v57, v37
	v_cvt_scalef32_pk_f16_fp4 v37, v186, 1.0 op_sel:[1,0,0]
	v_pk_fma_f16 v20, v45, v91, v20
	v_cvt_scalef32_pk_f16_fp4 v45, v157, 1.0 op_sel:[1,1,0]
	v_pk_fma_f16 v48, v48, v53, v49
	v_cvt_scalef32_pk_f16_fp4 v49, v153, 1.0 op_sel:[0,1,0]
	v_pk_fma_f16 v60, v60, v95, v61
	v_cvt_scalef32_pk_f16_fp4 v61, v149, 1.0 op_sel:[1,0,0]
	v_pk_fma_f16 v64, v64, v52, v65
	v_cvt_scalef32_pk_f16_fp4 v35, v145, 1.0
	v_pk_fma_f16 v19, v31, v96, v19
	v_cvt_scalef32_pk_f16_fp4 v25, v190, 1.0 op_sel:[1,1,0]
	v_pk_fma_f16 v37, v37, v57, v41
	v_cvt_scalef32_pk_f16_fp4 v41, v186, 1.0
	v_cvt_scalef32_pk_f16_fp4 v44, v161, 1.0 op_sel:[1,1,0]
	v_pk_fma_f16 v45, v45, v94, v48
	v_cvt_scalef32_pk_f16_fp4 v48, v157, 1.0 op_sel:[0,1,0]
	v_pk_fma_f16 v49, v49, v53, v60
	v_cvt_scalef32_pk_f16_fp4 v60, v153, 1.0 op_sel:[1,0,0]
	v_pk_fma_f16 v61, v61, v95, v64
	v_cvt_scalef32_pk_f16_fp4 v39, v149, 1.0
	v_pk_fma_f16 v19, v35, v52, v19
	v_pk_fma_f16 v25, v25, v90, v29
	v_cvt_scalef32_pk_f16_fp4 v29, v190, 1.0 op_sel:[0,1,0]
	v_pk_fma_f16 v20, v41, v57, v20
	v_cvt_scalef32_pk_f16_fp4 v41, v165, 1.0 op_sel:[1,1,0]
	v_pk_fma_f16 v44, v44, v54, v45
	v_cvt_scalef32_pk_f16_fp4 v45, v161, 1.0 op_sel:[0,1,0]
	v_pk_fma_f16 v48, v48, v94, v49
	v_cvt_scalef32_pk_f16_fp4 v49, v157, 1.0 op_sel:[1,0,0]
	v_pk_fma_f16 v60, v60, v53, v61
	v_cvt_scalef32_pk_f16_fp4 v43, v153, 1.0
	v_pk_fma_f16 v19, v39, v95, v19
	v_pk_fma_f16 v29, v29, v90, v33
	v_cvt_scalef32_pk_f16_fp4 v33, v190, 1.0 op_sel:[1,0,0]
	v_pk_fma_f16 v41, v41, v93, v44
	v_cvt_scalef32_pk_f16_fp4 v44, v165, 1.0 op_sel:[0,1,0]
	v_pk_fma_f16 v45, v45, v54, v48
	v_cvt_scalef32_pk_f16_fp4 v48, v161, 1.0 op_sel:[1,0,0]
	v_pk_fma_f16 v49, v49, v94, v60
	v_cvt_scalef32_pk_f16_fp4 v47, v157, 1.0
	v_pk_fma_f16 v19, v43, v53, v19
	v_pk_fma_f16 v33, v33, v90, v37
	v_cvt_scalef32_pk_f16_fp4 v37, v190, 1.0
	v_cvt_scalef32_pk_f16_fp4 v40, v169, 1.0 op_sel:[1,1,0]
	v_pk_fma_f16 v44, v44, v93, v45
	v_cvt_scalef32_pk_f16_fp4 v45, v165, 1.0 op_sel:[1,0,0]
	v_pk_fma_f16 v48, v48, v54, v49
	v_cvt_scalef32_pk_f16_fp4 v49, v161, 1.0
	v_pk_fma_f16 v19, v47, v94, v19
	v_cvt_scalef32_pk_f16_fp4 v59, v128, 1.0 op_sel:[1,1,0]
	v_pk_fma_f16 v20, v37, v90, v20
	v_cvt_scalef32_pk_f16_fp4 v37, v173, 1.0 op_sel:[1,1,0]
	v_pk_fma_f16 v40, v40, v55, v41
	v_cvt_scalef32_pk_f16_fp4 v41, v169, 1.0 op_sel:[0,1,0]
	v_pk_fma_f16 v45, v45, v93, v48
	v_cvt_scalef32_pk_f16_fp4 v48, v165, 1.0
	v_pk_fma_f16 v19, v49, v54, v19
	v_cvt_scalef32_pk_f16_fp4 v49, v132, 1.0 op_sel:[1,1,0]
	v_pk_fma_f16 v59, v59, v98, 0
	v_pk_fma_f16 v37, v37, v92, v40
	v_cvt_scalef32_pk_f16_fp4 v40, v173, 1.0 op_sel:[0,1,0]
	v_pk_fma_f16 v41, v41, v55, v44
	v_cvt_scalef32_pk_f16_fp4 v44, v169, 1.0 op_sel:[1,0,0]
	v_pk_fma_f16 v19, v48, v93, v19
	v_cvt_scalef32_pk_f16_fp4 v48, v136, 1.0 op_sel:[1,1,0]
	v_pk_fma_f16 v49, v49, v97, v59
	v_cvt_scalef32_pk_f16_fp4 v60, v128, 1.0 op_sel:[0,1,0]
	v_cvt_scalef32_pk_f16_fp4 v36, v177, 1.0 op_sel:[1,1,0]
	v_pk_fma_f16 v40, v40, v92, v41
	v_cvt_scalef32_pk_f16_fp4 v41, v173, 1.0 op_sel:[1,0,0]
	v_pk_fma_f16 v44, v44, v55, v45
	v_cvt_scalef32_pk_f16_fp4 v45, v169, 1.0
	v_cvt_scalef32_pk_f16_fp4 v47, v140, 1.0 op_sel:[1,1,0]
	v_pk_fma_f16 v48, v48, v51, v49
	v_cvt_scalef32_pk_f16_fp4 v59, v132, 1.0 op_sel:[0,1,0]
	v_pk_fma_f16 v60, v60, v98, 0
	v_cvt_scalef32_pk_f16_fp4 v61, v128, 1.0 op_sel:[1,0,0]
	v_cvt_scalef32_pk_f16_fp4 v32, v181, 1.0 op_sel:[1,1,0]
	v_pk_fma_f16 v36, v36, v56, v37
	v_cvt_scalef32_pk_f16_fp4 v37, v177, 1.0 op_sel:[0,1,0]
	v_pk_fma_f16 v41, v41, v92, v44
	v_cvt_scalef32_pk_f16_fp4 v44, v173, 1.0
	v_pk_fma_f16 v19, v45, v55, v19
	v_cvt_scalef32_pk_f16_fp4 v45, v144, 1.0 op_sel:[1,1,0]
	v_pk_fma_f16 v47, v47, v96, v48
	v_cvt_scalef32_pk_f16_fp4 v49, v136, 1.0 op_sel:[0,1,0]
	v_pk_fma_f16 v59, v59, v97, v60
	v_cvt_scalef32_pk_f16_fp4 v60, v132, 1.0 op_sel:[1,0,0]
	v_pk_fma_f16 v61, v61, v98, 0
	v_cvt_scalef32_pk_f16_fp4 v18, v128, 1.0
	v_cvt_scalef32_pk_f16_fp4 v28, v185, 1.0 op_sel:[1,1,0]
	v_pk_fma_f16 v32, v32, v91, v36
	v_cvt_scalef32_pk_f16_fp4 v36, v181, 1.0 op_sel:[0,1,0]
	v_pk_fma_f16 v37, v37, v56, v40
	v_cvt_scalef32_pk_f16_fp4 v40, v177, 1.0 op_sel:[1,0,0]
	v_pk_fma_f16 v19, v44, v92, v19
	v_cvt_scalef32_pk_f16_fp4 v44, v148, 1.0 op_sel:[1,1,0]
	v_pk_fma_f16 v45, v45, v52, v47
	v_cvt_scalef32_pk_f16_fp4 v48, v140, 1.0 op_sel:[0,1,0]
	v_pk_fma_f16 v49, v49, v51, v59
	v_cvt_scalef32_pk_f16_fp4 v59, v136, 1.0 op_sel:[1,0,0]
	v_pk_fma_f16 v60, v60, v97, v61
	v_cvt_scalef32_pk_f16_fp4 v22, v132, 1.0
	v_pk_fma_f16 v18, v18, v98, 0
	v_cvt_scalef32_pk_f16_fp4 v24, v189, 1.0 op_sel:[1,1,0]
	v_pk_fma_f16 v28, v28, v57, v32
	v_pk_fma_f16 v36, v36, v91, v37
	v_cvt_scalef32_pk_f16_fp4 v37, v181, 1.0 op_sel:[1,0,0]
	v_pk_fma_f16 v40, v40, v56, v41
	v_cvt_scalef32_pk_f16_fp4 v41, v177, 1.0
	v_cvt_scalef32_pk_f16_fp4 v43, v152, 1.0 op_sel:[1,1,0]
	v_pk_fma_f16 v44, v44, v95, v45
	v_cvt_scalef32_pk_f16_fp4 v47, v144, 1.0 op_sel:[0,1,0]
	v_pk_fma_f16 v48, v48, v96, v49
	v_cvt_scalef32_pk_f16_fp4 v49, v140, 1.0 op_sel:[1,0,0]
	v_pk_fma_f16 v59, v59, v51, v60
	v_cvt_scalef32_pk_f16_fp4 v26, v136, 1.0
	v_pk_fma_f16 v18, v22, v97, v18
	v_pk_fma_f16 v32, v24, v90, v28
	v_cvt_scalef32_pk_f16_fp4 v28, v185, 1.0 op_sel:[0,1,0]
	v_pk_fma_f16 v37, v37, v91, v40
	v_cvt_scalef32_pk_f16_fp4 v40, v181, 1.0
	v_pk_fma_f16 v19, v41, v56, v19
	v_cvt_scalef32_pk_f16_fp4 v41, v156, 1.0 op_sel:[1,1,0]
	v_pk_fma_f16 v43, v43, v53, v44
	v_cvt_scalef32_pk_f16_fp4 v45, v148, 1.0 op_sel:[0,1,0]
	v_pk_fma_f16 v47, v47, v52, v48
	v_cvt_scalef32_pk_f16_fp4 v48, v144, 1.0 op_sel:[1,0,0]
	v_pk_fma_f16 v49, v49, v96, v59
	v_cvt_scalef32_pk_f16_fp4 v30, v140, 1.0
	v_pk_fma_f16 v18, v26, v51, v18
	v_cvt_scalef32_pk_f16_fp4 v24, v189, 1.0 op_sel:[0,1,0]
	v_pk_fma_f16 v28, v28, v57, v36
	v_cvt_scalef32_pk_f16_fp4 v36, v185, 1.0 op_sel:[1,0,0]
	v_pk_fma_f16 v19, v40, v91, v19
	v_cvt_scalef32_pk_f16_fp4 v40, v160, 1.0 op_sel:[1,1,0]
	v_pk_fma_f16 v41, v41, v94, v43
	v_cvt_scalef32_pk_f16_fp4 v44, v152, 1.0 op_sel:[0,1,0]
	v_pk_fma_f16 v45, v45, v95, v47
	v_cvt_scalef32_pk_f16_fp4 v47, v148, 1.0 op_sel:[1,0,0]
	v_pk_fma_f16 v48, v48, v52, v49
	v_cvt_scalef32_pk_f16_fp4 v34, v144, 1.0
	v_pk_fma_f16 v18, v30, v96, v18
	v_pk_fma_f16 v24, v24, v90, v28
	v_cvt_scalef32_pk_f16_fp4 v28, v189, 1.0 op_sel:[1,0,0]
	v_pk_fma_f16 v36, v36, v57, v37
	v_cvt_scalef32_pk_f16_fp4 v37, v185, 1.0
	v_cvt_scalef32_pk_f16_fp4 v39, v164, 1.0 op_sel:[1,1,0]
	v_pk_fma_f16 v40, v40, v54, v41
	v_cvt_scalef32_pk_f16_fp4 v43, v156, 1.0 op_sel:[0,1,0]
	v_pk_fma_f16 v44, v44, v53, v45
	v_cvt_scalef32_pk_f16_fp4 v45, v152, 1.0 op_sel:[1,0,0]
	v_pk_fma_f16 v47, v47, v95, v48
	v_cvt_scalef32_pk_f16_fp4 v38, v148, 1.0
	v_pk_fma_f16 v18, v34, v52, v18
	v_pk_fma_f16 v28, v28, v90, v36
	v_cvt_scalef32_pk_f16_fp4 v36, v189, 1.0
	v_pk_fma_f16 v19, v37, v57, v19
	v_cvt_scalef32_pk_f16_fp4 v37, v168, 1.0 op_sel:[1,1,0]
	v_pk_fma_f16 v39, v39, v93, v40
	v_cvt_scalef32_pk_f16_fp4 v41, v160, 1.0 op_sel:[0,1,0]
	v_pk_fma_f16 v43, v43, v94, v44
	v_cvt_scalef32_pk_f16_fp4 v44, v156, 1.0 op_sel:[1,0,0]
	v_pk_fma_f16 v45, v45, v53, v47
	v_cvt_scalef32_pk_f16_fp4 v42, v152, 1.0
	v_pk_fma_f16 v18, v38, v95, v18
	v_pk_fma_f16 v35, v36, v90, v19
	v_cvt_scalef32_pk_f16_fp4 v36, v172, 1.0 op_sel:[1,1,0]
	v_pk_fma_f16 v37, v37, v55, v39
	v_cvt_scalef32_pk_f16_fp4 v40, v164, 1.0 op_sel:[0,1,0]
	v_pk_fma_f16 v41, v41, v54, v43
	v_cvt_scalef32_pk_f16_fp4 v43, v160, 1.0 op_sel:[1,0,0]
	v_pk_fma_f16 v44, v44, v94, v45
	v_cvt_scalef32_pk_f16_fp4 v45, v156, 1.0
	v_pk_fma_f16 v18, v42, v53, v18
	v_cvt_scalef32_pk_f16_fp4 v31, v176, 1.0 op_sel:[1,1,0]
	v_pk_fma_f16 v36, v36, v92, v37
	v_cvt_scalef32_pk_f16_fp4 v39, v168, 1.0 op_sel:[0,1,0]
	v_pk_fma_f16 v40, v40, v93, v41
	v_cvt_scalef32_pk_f16_fp4 v41, v164, 1.0 op_sel:[1,0,0]
	v_pk_fma_f16 v43, v43, v54, v44
	v_cvt_scalef32_pk_f16_fp4 v44, v160, 1.0
	v_pk_fma_f16 v18, v45, v94, v18
	v_cvt_scalef32_pk_f16_fp4 v27, v180, 1.0 op_sel:[1,1,0]
	v_pk_fma_f16 v31, v31, v56, v36
	v_cvt_scalef32_pk_f16_fp4 v37, v172, 1.0 op_sel:[0,1,0]
	v_pk_fma_f16 v39, v39, v55, v40
	v_cvt_scalef32_pk_f16_fp4 v40, v168, 1.0 op_sel:[1,0,0]
	v_pk_fma_f16 v41, v41, v93, v43
	v_cvt_scalef32_pk_f16_fp4 v43, v164, 1.0
	v_pk_fma_f16 v18, v44, v54, v18
	v_cvt_scalef32_pk_f16_fp4 v23, v184, 1.0 op_sel:[1,1,0]
	v_pk_fma_f16 v27, v27, v91, v31
	v_cvt_scalef32_pk_f16_fp4 v36, v176, 1.0 op_sel:[0,1,0]
	v_pk_fma_f16 v37, v37, v92, v39
	v_cvt_scalef32_pk_f16_fp4 v39, v172, 1.0 op_sel:[1,0,0]
	v_pk_fma_f16 v40, v40, v55, v41
	v_cvt_scalef32_pk_f16_fp4 v41, v168, 1.0
	v_pk_fma_f16 v18, v43, v93, v18
	v_cvt_scalef32_pk_f16_fp4 v19, v188, 1.0 op_sel:[1,1,0]
	v_pk_fma_f16 v23, v23, v57, v27
	v_cvt_scalef32_pk_f16_fp4 v27, v180, 1.0 op_sel:[0,1,0]
	v_pk_fma_f16 v36, v36, v56, v37
	v_cvt_scalef32_pk_f16_fp4 v37, v176, 1.0 op_sel:[1,0,0]
	v_pk_fma_f16 v39, v39, v92, v40
	v_cvt_scalef32_pk_f16_fp4 v40, v172, 1.0
	v_pk_fma_f16 v18, v41, v55, v18
	v_pk_fma_f16 v31, v19, v90, v23
	v_cvt_scalef32_pk_f16_fp4 v23, v184, 1.0 op_sel:[0,1,0]
	v_pk_fma_f16 v27, v27, v91, v36
	v_cvt_scalef32_pk_f16_fp4 v36, v180, 1.0 op_sel:[1,0,0]
	v_pk_fma_f16 v37, v37, v56, v39
	v_cvt_scalef32_pk_f16_fp4 v39, v176, 1.0
	v_pk_fma_f16 v18, v40, v92, v18
	v_cvt_scalef32_pk_f16_fp4 v19, v188, 1.0 op_sel:[0,1,0]
	v_pk_fma_f16 v23, v23, v57, v27
	v_cvt_scalef32_pk_f16_fp4 v27, v184, 1.0 op_sel:[1,0,0]
	v_pk_fma_f16 v36, v36, v91, v37
	v_cvt_scalef32_pk_f16_fp4 v37, v180, 1.0
	v_pk_fma_f16 v18, v39, v56, v18
	v_pk_fma_f16 v23, v19, v90, v23
	v_cvt_scalef32_pk_f16_fp4 v19, v188, 1.0 op_sel:[1,0,0]
	v_pk_fma_f16 v27, v27, v57, v36
	v_cvt_scalef32_pk_f16_fp4 v36, v184, 1.0
	v_pk_fma_f16 v18, v37, v91, v18
	v_pk_fma_f16 v27, v19, v90, v27
	v_cvt_scalef32_pk_f16_fp4 v19, v188, 1.0
	v_pk_fma_f16 v18, v36, v57, v18
	v_permlane32_swap_b32_e32 v27, v33
	v_pk_fma_f16 v18, v19, v90, v18
	v_permlane32_swap_b32_e32 v23, v29
	s_nop 0
	v_permlane32_swap_b32_e32 v18, v20
	v_pk_add_f16 v19, v18, v20
	v_pk_add_f16 v20, v27, v33
	v_permlane32_swap_b32_e32 v31, v25
	v_cvt_f32_f16_e32 v26, v20
	v_cvt_f32_f16_sdwa v27, v20 dst_sel:DWORD dst_unused:UNUSED_PAD src0_sel:WORD_1
	v_pk_add_f16 v20, v23, v29
	v_permlane32_swap_b32_e32 v28, v100
	v_cvt_f32_f16_e32 v22, v20
	v_cvt_f32_f16_sdwa v23, v20 dst_sel:DWORD dst_unused:UNUSED_PAD src0_sel:WORD_1
	v_pk_add_f16 v20, v31, v25
	v_permlane32_swap_b32_e32 v35, v21
	v_pk_add_f16 v25, v28, v100
	v_permlane32_swap_b32_e32 v24, v99
	v_permlane32_swap_b32_e32 v32, v50
	v_pk_add_f16 v21, v35, v21
	v_cvt_f32_f16_e32 v28, v25
	v_cvt_f32_f16_sdwa v29, v25 dst_sel:DWORD dst_unused:UNUSED_PAD src0_sel:WORD_1
	v_pk_add_f16 v25, v24, v99
	v_pk_add_f16 v33, v32, v50
	v_cvt_f32_f16_e32 v18, v19
	v_cvt_f32_f16_sdwa v19, v19 dst_sel:DWORD dst_unused:UNUSED_PAD src0_sel:WORD_1
	v_cvt_f32_f16_e32 v30, v20
	v_cvt_f32_f16_sdwa v31, v20 dst_sel:DWORD dst_unused:UNUSED_PAD src0_sel:WORD_1
	v_cvt_f32_f16_e32 v20, v21
	v_cvt_f32_f16_sdwa v21, v21 dst_sel:DWORD dst_unused:UNUSED_PAD src0_sel:WORD_1
	v_cvt_f32_f16_e32 v24, v25
	v_cvt_f32_f16_sdwa v25, v25 dst_sel:DWORD dst_unused:UNUSED_PAD src0_sel:WORD_1
	v_cvt_f32_f16_e32 v32, v33
	v_cvt_f32_f16_sdwa v33, v33 dst_sel:DWORD dst_unused:UNUSED_PAD src0_sel:WORD_1
	v_mul_hi_i32 v34, v110, s69
	v_lshrrev_b32_e32 v35, 31, v34
	v_ashrrev_i32_e32 v34, 13, v34
	v_add_u32_e32 v35, v34, v35
	v_permlane16_swap_b32_e32 v18, v20
	v_permlane16_swap_b32_e32 v19, v21
	v_permlane16_swap_b32_e32 v26, v28
	v_permlane16_swap_b32_e32 v27, v29
	v_permlane16_swap_b32_e32 v22, v24
	v_permlane16_swap_b32_e32 v23, v25
	v_permlane16_swap_b32_e32 v30, v32
	v_permlane16_swap_b32_e32 v31, v33
	v_mad_i32_i24 v34, v35, s20, v112
	v_pk_add_f32 v[20:21], v[18:19], v[20:21]
	v_pk_add_f32 v[18:19], v[22:23], v[24:25]
	v_pk_add_f32 v[28:29], v[26:27], v[28:29]
	v_pk_add_f32 v[26:27], v[30:31], v[32:33]
	v_add3_u32 v34, v34, s33, 1
	v_mov_b32_dpp v24, v20 row_ror:8 row_mask:0xf bank_mask:0xf bound_ctrl:1
	v_mov_b32_dpp v22, v18 row_ror:8 row_mask:0xf bank_mask:0xf bound_ctrl:1
	v_mov_b32_dpp v25, v21 row_ror:8 row_mask:0xf bank_mask:0xf bound_ctrl:1
	v_mov_b32_dpp v23, v19 row_ror:8 row_mask:0xf bank_mask:0xf bound_ctrl:1
	v_mov_b32_dpp v32, v28 row_ror:8 row_mask:0xf bank_mask:0xf bound_ctrl:1
	v_mov_b32_dpp v30, v26 row_ror:8 row_mask:0xf bank_mask:0xf bound_ctrl:1
	v_mov_b32_dpp v33, v29 row_ror:8 row_mask:0xf bank_mask:0xf bound_ctrl:1
	v_mov_b32_dpp v31, v27 row_ror:8 row_mask:0xf bank_mask:0xf bound_ctrl:1
	v_mul_i32_i24_e32 v38, 0xffffbf00, v35
	v_cmp_gt_i32_e32 vcc, s68, v34
	v_cmp_lt_i32_e64 s[0:1], s21, v34
	s_and_saveexec_b64 s[2:3], s[0:1]
	s_xor_b64 s[0:1], exec, s[2:3]
	v_lshl_add_u32 v34, v35, 14, v38
	s_movk_i32 s2, 0xff01
	v_add3_u32 v34, v113, v34, s2
	s_or_saveexec_b64 s[0:1], s[0:1]
	v_mov_b64_e32 v[36:37], s[18:19]
	s_xor_b64 exec, exec, s[0:1]
	s_cbranch_execz .LBB0_888
	v_add_u32_e32 v34, v38, v113
	v_lshlrev_b32_e32 v36, 8, v35
	v_add3_u32 v34, v34, v36, 1
	v_mov_b64_e32 v[36:37], s[72:73]
	s_branch .LBB0_888
